# attention diff-subhead body: K/V tiles staged by LDS-DMA (global_load_lds) instead of global_load+ds_write
# speedup vs baseline: 1.0063x; 1.0063x over previous
; __device__ __forceinline__ unsigned cvtpk(float lo, float hi) { unsigned r; asm volatile("v_cvt_pk_bf16_f32 %0, %1, %2" : "=v"(r) : "v"(lo), "v"(hi)); return r; }
; __device__ __forceinline__ int v_st(int k, int c) { const int kk = (k & ~0xC) | ((k & 4) << 1) | ((k & 8) >> 1); return ((kk >> 3) * 4 + (c >> 5)) * 512 + ((kk & 7) * 32 + (c & 31)) * 2; }
; __device__ __forceinline__ int v_rd_base(int lane) { return ((lane & 3) << 3) | (((lane >> 2) & 3) << 6) | (((lane >> 4) & 1) << 5) | (((lane >> 5) & 1) << 8); }
; #define SWRITE(b, i) do { *(LAS bf16x8*)(V_lds + (b) * SHM_V + vst0) = sr_[i].vs0;          \
;     *(LAS bf16x8*)(V_lds + (b) * SHM_V + vst1) = sr_[i].vs1; int kc = sc * 2;               \
;     *(LAS bf16x8*)(K_lds + (b) * SHM_K + KSWZ(sr, kc)) = sr_[i].ks0;                       \
;     *(LAS bf16x8*)(K_lds + (b) * SHM_K + KSWZ(32 + sr, kc)) = sr_[i].ks1; } while (0)
; template <bool HALF> __device__ __forceinline__ void dense_body(const bf16_t* __restrict__ Qb, const bf16_t* __restrict__ Kh, const bf16_t* __restrict__ Vh, ...
;     ...
;     for (int d0 = 0; d0 < NQ; ++d0) { u32x4 w;
; #pragma unroll
;       for (int j = 0; j < 4; ++j) w[j] = cvtpk(qf[d0][2 * j], qf[d0][2 * j + 1]);
;       qr[d0] = *reinterpret_cast<bf16x8*>(&w); } }
;   const int sr = tid >> 4, sc = (tid & 15) * 8, vst0 = v_st(sr, sc), vst1 = v_st(32 + sr, sc);
;   const int vb0 = (int)(uintptr_t)V_lds + v_rd_base(lane);
;   struct { bf16x8 vs0, vs1, ks0, ks1; } sr_[2];
;   const unsigned ko0 = (unsigned)(sr * LDKK + sc) * 2u, ko1 = ko0 + 32u * LDKK * 2u, vo0 = (unsigned)(sr * LDKV + sc) * 2u, vo1 = vo0 + 32u * LDKV * 2u;
;     ...
;   f32x16 pA0, pA1, pB0, pB1; float mnA, mnB, alA, alB; bf16x8 pa0, pa1, pa2, pa3; const int NT = seq / KVBLK;
;   const char* Kl0 = (const char*)K_lds; const char* Kl1 = (const char*)(K_lds + SHM_K);
;   constexpr int SE = 0, SO = 1;
;   SLOAD(SE, 0); asm volatile("s_waitcnt vmcnt(0)" ::: "memory"); SWRITE(0, SE); __syncthreads();
;   qkt<HALF>(pA0, pA1, Kl0, qr, r32, hi, koff); partialSM(pA0, pA1, m_reg, mnA, alA);
.LBB0_424:
	s_ashr_i32 s6, s2, 2
	s_add_i32 s2, s2, -8
	s_lshr_b32 s2, s2, 1
	s_add_i32 s7, s2, 2
	s_and_b64 s[2:3], s[20:21], exec
	s_cselect_b32 s3, s6, s7
	s_lshl_b32 s2, s3, 7
	s_cmp_lt_i32 s3, 2
	s_movk_i32 s3, 0x1100
	s_cselect_b32 s3, s3, 0x1500
	s_add_i32 s6, s3, s2
	s_ashr_i32 s3, s2, 31
	s_lshl_b64 s[20:21], s[2:3], 1
	s_add_u32 s34, s44, s20
	v_cvt_pk_bf16_f32 v118, v122, v36
	v_cvt_pk_bf16_f32 v119, v123, v37
	v_cvt_pk_bf16_f32 v120, v120, v28
	v_cvt_pk_bf16_f32 v121, v121, v29
	v_cvt_pk_bf16_f32 v126, v114, v32
	v_cvt_pk_bf16_f32 v127, v115, v33
	v_cvt_pk_bf16_f32 v128, v112, v24
	v_cvt_pk_bf16_f32 v129, v113, v25
	v_cvt_pk_bf16_f32 v122, v108, v26
	v_cvt_pk_bf16_f32 v123, v109, v27
	v_cvt_pk_bf16_f32 v124, v106, v20
	v_cvt_pk_bf16_f32 v125, v107, v21
	v_cvt_pk_bf16_f32 v114, v104, v22
	v_cvt_pk_bf16_f32 v115, v105, v23
	v_cvt_pk_bf16_f32 v116, v74, v16
	v_cvt_pk_bf16_f32 v117, v75, v17
	v_ashrrev_i32_e32 v16, 4, v142
	v_lshlrev_b32_e32 v17, 3, v142
	s_movk_i32 s2, 0x300
	s_addc_u32 s35, s45, s21
	s_ashr_i32 s7, s6, 31
	v_cvt_pk_bf16_f32 v110, v72, v18
	v_and_b32_e32 v18, 0x78, v17
	v_mul_lo_u32 v0, v16, s2
	s_movk_i32 s2, 0x1800
	s_lshl_b64 s[22:23], s[6:7], 1
	v_cvt_pk_bf16_f32 v111, v73, v19
	v_cvt_pk_bf16_f32 v112, v70, v12
	v_cvt_pk_bf16_f32 v113, v71, v13
	v_cvt_pk_bf16_f32 v106, v68, v14
	v_cvt_pk_bf16_f32 v107, v69, v15
	v_cvt_pk_bf16_f32 v108, v6, v8
	v_or_b32_e32 v8, v0, v18
	v_mul_lo_u32 v0, v16, s2
	s_add_u32 s38, s30, s22
	v_or_b32_e32 v0, v0, v18
	s_addc_u32 s39, s31, s23
	v_lshlrev_b32_e32 v50, 1, v0
	v_cvt_pk_bf16_f32 v109, v7, v9
	v_cvt_pk_bf16_f32 v102, v4, v10
	v_cvt_pk_bf16_f32 v103, v5, v11
	v_cvt_pk_bf16_f32 v104, v2, v64
	v_cvt_pk_bf16_f32 v105, v1, v65
	v_cvt_pk_bf16_f32 v98, v40, v46
	v_cvt_pk_bf16_f32 v99, v39, v47
	v_cvt_pk_bf16_f32 v100, v34, v42
	v_cvt_pk_bf16_f32 v101, v31, v43
	v_add_u32_e32 v48, 0x60000, v50
	global_load_dwordx4 v[0:3], v50, s[38:39]
	global_load_dwordx4 v[4:7], v48, s[38:39]
	v_lshlrev_b32_e32 v52, 1, v8
	global_load_dwordx4 v[8:11], v52, s[34:35]
	v_add_u32_e32 v54, 0xc000, v52
	global_load_dwordx4 v[12:15], v54, s[34:35]
	v_and_b32_e32 v20, 0xfffff0, v16
	v_lshlrev_b32_e32 v21, 1, v16
	v_lshrrev_b32_e32 v22, 1, v16
	v_and_b32_e32 v23, 3, v16
	v_add_u32_e32 v24, 32, v16
	v_and_or_b32 v20, v21, 8, v20
	v_and_or_b32 v21, v22, 4, v23
	v_and_b32_e32 v22, 0xfffff0, v24
	v_lshlrev_b32_e32 v23, 1, v24
	v_bfe_u32 v17, v17, 5, 2
	v_lshrrev_b32_e32 v20, 1, v20
	v_and_or_b32 v22, v23, 8, v22
	v_lshlrev_b32_e32 v18, 1, v18
	v_or_b32_e32 v20, v20, v17
	v_lshrrev_b32_e32 v22, 1, v22
	v_lshlrev_b32_e32 v21, 6, v21
	v_and_b32_e32 v25, 48, v18
	v_lshlrev_b32_e32 v20, 9, v20
	v_or_b32_e32 v17, v22, v17
	v_or3_b32 v20, v20, v21, v25
	v_lshlrev_b32_e32 v17, 9, v17
	v_or3_b32 v17, v17, v21, v25
	v_add_u32_e32 v205, 0, v20
	v_and_b32_e32 v19, 0x70, v142
	v_lshlrev_b32_e32 v16, 8, v16
	v_add_u32_e32 v206, 0, v17
	s_waitcnt vmcnt(0)
	v_bitop3_b32 v16, v18, v16, v19 bitop3:0xde
	s_waitcnt vmcnt(3)
	ds_write_b128 v205, v[0:3]
	s_waitcnt vmcnt(2)
	ds_write_b128 v206, v[4:7]
	v_lshlrev_b32_e32 v0, 8, v24
	v_bitop3_b32 v0, v18, v0, v19 bitop3:0xde
	v_add_u32_e32 v207, 0, v16
	v_add_u32_e32 v208, 0, v0
	v_lshlrev_b32_e32 v0, 4, v197
	s_waitcnt vmcnt(1)
	ds_write_b128 v207, v[8:11] offset:32768
	v_lshlrev_b32_e32 v8, 8, v197
	v_and_b32_e32 v9, 0x70, v0
	v_bitop3_b32 v0, v96, v8, v9 bitop3:0xde
	v_add_u32_e32 v209, 0, v0
	s_waitcnt vmcnt(0)
	ds_write_b128 v208, v[12:15] offset:32768
	s_waitcnt lgkmcnt(0)
	s_barrier
	ds_read_b128 v[0:3], v209 offset:32768
	ds_read_b128 v[4:7], v209 offset:40960
	s_waitcnt lgkmcnt(1)
	v_mfma_f32_32x32x16_bf16 v[16:31], v[0:3], v[118:121], 0
	v_or_b32_e32 v0, 32, v96
	v_bitop3_b32 v0, v0, v8, v9 bitop3:0xde
	v_add_u32_e32 v221, 0, v0
	v_and_b32_e32 v76, 63, v142
	v_and_b32_e32 v10, 0x3fffffc0, v142
	s_add_i32 s46, 0, 0x10000
	v_lshl_add_u32 v200, v10, 2, s46
	s_waitcnt lgkmcnt(0)
	v_mfma_f32_32x32x16_bf16 v[32:47], v[4:7], v[118:121], 0
	ds_read_b128 v[0:3], v221 offset:32768
	ds_read_b128 v[4:7], v221 offset:40960
	v_lshlrev_b32_e32 v10, 3, v76
	s_add_u32 s6, s34, 0x18000
	s_addc_u32 s7, s35, 0
	s_add_u32 s16, s38, 0xc0000
	s_addc_u32 s17, s39, 0
	s_mov_b32 s64, s65
	s_waitcnt lgkmcnt(1)
	v_mfma_f32_32x32x16_bf16 v[16:31], v[0:3], v[126:129], v[16:31]
	v_or_b32_e32 v0, 64, v96
	v_bitop3_b32 v0, v0, v8, v9 bitop3:0xde
	v_add_u32_e32 v222, 0, v0
	s_mov_b32 s66, s65
	s_mov_b32 s67, s65
	s_mov_b32 s68, s65
	s_mov_b32 s69, s65
	s_waitcnt lgkmcnt(0)
	v_mfma_f32_32x32x16_bf16 v[32:47], v[4:7], v[126:129], v[32:47]
	ds_read_b128 v[0:3], v222 offset:32768
	ds_read_b128 v[4:7], v222 offset:40960
	s_mov_b32 s70, s65
	s_mov_b32 s71, s65
	s_mov_b32 s72, s65
	s_mov_b32 s73, s65
	s_mov_b32 s74, s65
	s_mov_b32 s75, s65
	s_waitcnt lgkmcnt(1)
	v_mfma_f32_32x32x16_bf16 v[16:31], v[0:3], v[122:125], v[16:31]
	v_or_b32_e32 v0, 0x60, v96
	v_bitop3_b32 v0, v0, v8, v9 bitop3:0xde
	v_add_u32_e32 v210, 0, v0
	s_mov_b32 s76, s65
	s_mov_b32 s77, s65
	s_mov_b32 s78, s65
	s_mov_b32 s79, s65
	s_waitcnt lgkmcnt(0)
	v_mfma_f32_32x32x16_bf16 v[32:47], v[4:7], v[122:125], v[32:47]
	ds_read_b128 v[0:3], v210 offset:32768
	ds_read_b128 v[4:7], v210 offset:40960
	v_mov_b32_e32 v51, v97
	v_mov_b32_e32 v49, v97
	v_mov_b32_e32 v53, v97
	v_mov_b32_e32 v55, v97
	v_lshl_add_u64 v[180:181], s[22:23], 0, v[50:51]
	v_lshl_add_u64 v[182:183], s[22:23], 0, v[48:49]
	s_waitcnt lgkmcnt(1)
	v_mfma_f32_32x32x16_bf16 v[16:31], v[0:3], v[114:117], v[16:31]
	v_or_b32_e32 v0, 0x80, v96
	v_bitop3_b32 v0, v0, v8, v9 bitop3:0xde
	v_add_u32_e32 v211, 0, v0
	ds_read_b128 v[0:3], v211 offset:32768
	v_lshl_add_u64 v[184:185], s[20:21], 0, v[52:53]
	v_lshl_add_u64 v[186:187], s[20:21], 0, v[54:55]
	s_mov_b32 s2, 4
	s_waitcnt lgkmcnt(1)
; __device__ __forceinline__ void partialSM(f32x16& p0, f32x16& p1, float& m_reg, float& mn, float& alpha) {
;   constexpr float C = SCALE * 1.4426950408889634f;
;   float pmax = p0[0]; for (int r = 1; r < 16; ++r) pmax = fmaxf(pmax, p0[r]); for (int r = 0; r < 16; ++r) pmax = fmaxf(pmax, p1[r]);
;   { auto rr = __builtin_amdgcn_permlane32_swap(__float_as_uint(pmax), __float_as_uint(pmax), false, false);
;     pmax = fmaxf(__uint_as_float(rr[0]), __uint_as_float(rr[1])); }
;   if (__builtin_expect(__all(pmax - m_reg <= THR / SCALE), 1)) { mn = m_reg; alpha = 1.f; }
;   else { mn = fmaxf(m_reg, pmax); alpha = __builtin_amdgcn_exp2f((m_reg - mn) * C); m_reg = mn; }
;   float mnC = -mn * C;
;   for (int r = 0; r < 16; ++r) p0[r] = fmaf(p0[r], C, mnC); for (int r = 0; r < 16; ++r) p1[r] = fmaf(p1[r], C, mnC);
;   for (int r = 0; r < 16; ++r) p0[r] = __builtin_amdgcn_exp2f(p0[r]);
; }
; template <bool HALF> __device__ __forceinline__ void qkt(f32x16& p0, f32x16& p1, const char* Ks, const bf16x8* qr, int r32, int hi, int koff) {
;   p0 = f32x16{}; p1 = f32x16{};
;   for (int d0 = 0; d0 < (HALF ? 4 : 8); ++d0) { int cb = (d0 * 16 + hi * 8) * 2 + koff;
;     bf16x8 b0 = *reinterpret_cast<const bf16x8*>(Ks + KSWZ(r32, cb));
;     bf16x8 b1 = *reinterpret_cast<const bf16x8*>(Ks + KSWZ(32 + r32, cb));
;     p0 = __builtin_amdgcn_mfma_f32_32x32x16_bf16(b0, qr[d0], p0, 0, 0, 0);
;     p1 = __builtin_amdgcn_mfma_f32_32x32x16_bf16(b1, qr[d0], p1, 0, 0, 0); }
	v_mfma_f32_32x32x16_bf16 v[32:47], v[4:7], v[114:117], v[32:47]
	ds_read_b128 v[4:7], v211 offset:40960
	v_cmp_gt_u32_e64 s[40:41], 32, v76
	v_lshl_add_u32 v201, v197, 2, v200
	v_mov_b32_e32 v202, 0
	s_waitcnt lgkmcnt(1)
	v_mfma_f32_32x32x16_bf16 v[16:31], v[0:3], v[110:113], v[16:31]
	v_lshlrev_b32_e32 v0, 4, v76
	v_and_b32_e32 v0, 0xc0, v0
	v_and_or_b32 v11, v10, 24, v0
	v_or_b32_e32 v0, 0xa0, v96
	v_bitop3_b32 v0, v0, v8, v9 bitop3:0xde
	v_add_u32_e32 v223, 0, v0
	v_and_b32_e32 v10, 0x100, v10
	s_waitcnt lgkmcnt(0)
	v_mfma_f32_32x32x16_bf16 v[32:47], v[4:7], v[110:113], v[32:47]
	ds_read_b128 v[0:3], v223 offset:32768
	ds_read_b128 v[4:7], v223 offset:40960
	global_load_dwordx4 v[56:59], v50, s[16:17]
	global_load_dwordx4 v[60:63], v48, s[16:17]
	global_load_dwordx4 v[64:67], v52, s[6:7]
	global_load_dwordx4 v[68:71], v54, s[6:7]
	s_add_u32 s6, s34, 0x30000
	s_addc_u32 s7, s35, 0
	s_waitcnt lgkmcnt(1)
	v_mfma_f32_32x32x16_bf16 v[16:31], v[0:3], v[106:109], v[16:31]
	v_lshlrev_b32_e32 v0, 1, v76
	v_and_b32_e32 v12, 32, v0
	v_or_b32_e32 v0, 0xc0, v96
	v_bitop3_b32 v0, v0, v8, v9 bitop3:0xde
	v_add_u32_e32 v225, 0, v0
	ds_read_b128 v[0:3], v225 offset:32768
	v_or3_b32 v77, v11, v12, v10
	s_waitcnt lgkmcnt(1)
	v_mfma_f32_32x32x16_bf16 v[32:47], v[4:7], v[106:109], v[32:47]
	ds_read_b128 v[4:7], v225 offset:40960
	v_add_u32_e32 v204, 0, v77
	s_waitcnt lgkmcnt(1)
	v_mfma_f32_32x32x16_bf16 v[16:31], v[0:3], v[102:105], v[16:31]
	v_or_b32_e32 v0, 0xe0, v96
	v_bitop3_b32 v0, v0, v8, v9 bitop3:0xde
	v_add_u32_e32 v224, 0, v0
	ds_read_b128 v[0:3], v224 offset:32768
	ds_read_b128 v[72:75], v224 offset:40960
	global_load_dwordx4 v[142:145], v54, s[6:7]
	global_load_dwordx4 v[138:141], v52, s[6:7]
	s_add_u32 s6, s38, 0x180000
	s_addc_u32 s7, s39, 0
	global_load_dwordx4 v[134:137], v48, s[6:7]
	global_load_dwordx4 v[130:133], v50, s[6:7]
	s_waitcnt lgkmcnt(2)
	v_mfma_f32_32x32x16_bf16 v[32:47], v[4:7], v[102:105], v[32:47]
	s_waitcnt vmcnt(4)
	s_waitcnt vmcnt(7)
	ds_write_b128 v205, v[56:59] offset:16384
	s_waitcnt vmcnt(6)
	ds_write_b128 v206, v[60:63] offset:16384
	s_waitcnt vmcnt(5)
	ds_write_b128 v207, v[64:67] offset:49152
	s_waitcnt vmcnt(4)
	ds_write_b128 v208, v[68:71] offset:49152
	s_waitcnt lgkmcnt(5)
	v_mfma_f32_32x32x16_bf16 v[16:31], v[0:3], v[98:101], v[16:31]
	v_mov_b64_e32 v[0:1], s[64:65]
	v_mov_b64_e32 v[14:15], s[78:79]
	v_mov_b64_e32 v[2:3], s[66:67]
	v_mov_b64_e32 v[4:5], s[68:69]
	v_mov_b64_e32 v[6:7], s[70:71]
	v_mov_b64_e32 v[8:9], s[72:73]
	v_mov_b64_e32 v[10:11], s[74:75]
	s_waitcnt lgkmcnt(4)
	v_mfma_f32_32x32x16_bf16 v[32:47], v[72:75], v[98:101], v[32:47]
	s_nop 2
	v_max_f32_e32 v72, v17, v17
	v_max_f32_e32 v73, v16, v16
	v_max_f32_e32 v72, v73, v72
	v_max3_f32 v72, v72, v18, v19
	v_max3_f32 v72, v72, v20, v21
	v_max3_f32 v72, v72, v22, v23
	v_max3_f32 v72, v72, v24, v25
	v_max3_f32 v72, v72, v26, v27
	v_max3_f32 v72, v72, v28, v29
	v_max3_f32 v72, v72, v30, v31
	v_max3_f32 v72, v72, v32, v33
	v_max3_f32 v72, v72, v34, v35
	v_max3_f32 v72, v72, v36, v37
	v_max3_f32 v72, v72, v38, v39
	v_max3_f32 v72, v72, v40, v41
	v_max3_f32 v72, v72, v42, v43
	v_max3_f32 v72, v72, v44, v45
	v_max3_f32 v72, v72, v46, v47
	v_mov_b32_e32 v73, v72
	s_nop 1
	v_permlane32_swap_b32_e32 v72, v73
	v_max_f32_e32 v73, v73, v73
	v_max_f32_e32 v72, v72, v72
	v_max_f32_e32 v72, v72, v73
	v_add_f32_e32 v73, 0x7149f2ca, v72
	v_cmp_ge_f32_e32 vcc, s87, v73
	s_cmp_eq_u64 vcc, exec
	v_max_f32_e32 v56, 0xf149f2ca, v72
	s_cselect_b64 vcc, -1, 0
	v_cndmask_b32_e32 v170, v56, v217, vcc
	v_sub_f32_e32 v57, 0xf149f2ca, v56
	v_mul_f32_e32 v56, 0xbe0293ee, v170
	v_fmamk_f32 v16, v16, 0x3e0293ee, v56
	v_exp_f32_e32 v163, v16
	v_fmamk_f32 v16, v17, 0x3e0293ee, v56
	v_exp_f32_e32 v177, v16
	v_fmamk_f32 v16, v18, 0x3e0293ee, v56
	v_exp_f32_e32 v164, v16
	v_fmamk_f32 v16, v19, 0x3e0293ee, v56
	v_exp_f32_e32 v188, v16
	v_fmamk_f32 v16, v20, 0x3e0293ee, v56
	v_exp_f32_e32 v176, v16
	v_fmamk_f32 v16, v21, 0x3e0293ee, v56
	v_exp_f32_e32 v189, v16
	v_fmamk_f32 v16, v22, 0x3e0293ee, v56
	v_exp_f32_e32 v165, v16
	v_fmamk_f32 v16, v23, 0x3e0293ee, v56
	v_exp_f32_e32 v175, v16
	v_fmamk_f32 v16, v24, 0x3e0293ee, v56
	v_mul_f32_e32 v57, 0x3e0293ee, v57
	v_exp_f32_e32 v166, v16
	v_fmamk_f32 v16, v25, 0x3e0293ee, v56
	v_exp_f32_e32 v57, v57
	v_exp_f32_e32 v173, v16
	v_fmamk_f32 v16, v26, 0x3e0293ee, v56
	v_exp_f32_e32 v167, v16
	v_fmamk_f32 v16, v27, 0x3e0293ee, v56
	v_exp_f32_e32 v174, v16
	v_fmamk_f32 v16, v28, 0x3e0293ee, v56
	v_exp_f32_e32 v168, v16
	v_fmamk_f32 v16, v29, 0x3e0293ee, v56
	v_pk_fma_f32 v[146:147], v[46:47], s[10:11], v[56:57] op_sel_hi:[1,0,0]
	v_pk_fma_f32 v[152:153], v[44:45], s[10:11], v[56:57] op_sel_hi:[1,0,0]
	v_pk_fma_f32 v[156:157], v[42:43], s[10:11], v[56:57] op_sel_hi:[1,0,0]
	v_pk_fma_f32 v[148:149], v[40:41], s[10:11], v[56:57] op_sel_hi:[1,0,0]
	v_pk_fma_f32 v[150:151], v[38:39], s[10:11], v[56:57] op_sel_hi:[1,0,0]
	v_pk_fma_f32 v[154:155], v[36:37], s[10:11], v[56:57] op_sel_hi:[1,0,0]
	v_pk_fma_f32 v[158:159], v[34:35], s[10:11], v[56:57] op_sel_hi:[1,0,0]
	v_pk_fma_f32 v[160:161], v[32:33], s[10:11], v[56:57] op_sel_hi:[1,0,0]
	v_exp_f32_e32 v171, v16
	v_fmamk_f32 v16, v30, 0x3e0293ee, v56
	v_fmac_f32_e32 v56, 0x3e0293ee, v31
	v_exp_f32_e32 v169, v16
	v_exp_f32_e32 v172, v56
	v_mov_b64_e32 v[12:13], s[76:77]
	v_cndmask_b32_e64 v226, v57, 1.0, vcc
	s_add_i32 s34, 0, 0x4000
	v_mov_b64_e32 v[62:63], v[14:15]
	v_mov_b64_e32 v[46:47], v[14:15]
	v_mov_b64_e32 v[30:31], v[14:15]
	v_add_u32_e32 v203, s34, v77
	v_mov_b64_e32 v[60:61], v[12:13]
	v_mov_b64_e32 v[58:59], v[10:11]
	v_mov_b64_e32 v[56:57], v[8:9]
	v_mov_b64_e32 v[54:55], v[6:7]
	v_mov_b64_e32 v[52:53], v[4:5]
	v_mov_b64_e32 v[50:51], v[2:3]
	v_mov_b64_e32 v[48:49], v[0:1]
	v_mov_b64_e32 v[44:45], v[12:13]
	v_mov_b64_e32 v[42:43], v[10:11]
	v_mov_b64_e32 v[40:41], v[8:9]
	v_mov_b64_e32 v[38:39], v[6:7]
	v_mov_b64_e32 v[36:37], v[4:5]
	v_mov_b64_e32 v[34:35], v[2:3]
	v_mov_b64_e32 v[32:33], v[0:1]
	v_mov_b64_e32 v[28:29], v[12:13]
	v_mov_b64_e32 v[26:27], v[10:11]
	v_mov_b64_e32 v[24:25], v[8:9]
	v_mov_b64_e32 v[22:23], v[6:7]
	v_mov_b64_e32 v[20:21], v[4:5]
	v_mov_b64_e32 v[18:19], v[2:3]
	v_mov_b64_e32 v[16:17], v[0:1]
	s_waitcnt lgkmcnt(0)
	s_barrier

; __device__ __forceinline__ int v_st(int k, int c) { const int kk = (k & ~0xC) | ((k & 4) << 1) | ((k & 8) >> 1); return ((kk >> 3) * 4 + (c >> 5)) * 512 + ((kk & 7) * 32 + (c & 31)) * 2; }
; __device__ __forceinline__ int v_rd_base(int lane) { return ((lane & 3) << 3) | (((lane >> 2) & 3) << 6) | (((lane >> 4) & 1) << 5) | (((lane >> 5) & 1) << 8); }
; #define SWRITE(b, i) do { *(LAS bf16x8*)(V_lds + (b) * SHM_V + vst0) = sr_[i].vs0;          \
;     *(LAS bf16x8*)(V_lds + (b) * SHM_V + vst1) = sr_[i].vs1; int kc = sc * 2;               \
;     *(LAS bf16x8*)(K_lds + (b) * SHM_K + KSWZ(sr, kc)) = sr_[i].ks0;                       \
;     *(LAS bf16x8*)(K_lds + (b) * SHM_K + KSWZ(32 + sr, kc)) = sr_[i].ks1; } while (0)
; #define SWAIT() asm volatile("s_waitcnt vmcnt(4)" ::: "memory")
; template <bool HALF> __device__ __forceinline__ void dense_body(const bf16_t* __restrict__ Qb, const bf16_t* __restrict__ Kh, const bf16_t* __restrict__ Vh, ...
;     ...
;   const int sr = tid >> 4, sc = (tid & 15) * 8, vst0 = v_st(sr, sc), vst1 = v_st(32 + sr, sc);
;   const int vb0 = (int)(uintptr_t)V_lds + v_rd_base(lane);
;   struct { bf16x8 vs0, vs1, ks0, ks1; } sr_[2];
;   const unsigned ko0 = (unsigned)(sr * LDKK + sc) * 2u, ko1 = ko0 + 32u * LDKK * 2u, vo0 = (unsigned)(sr * LDKV + sc) * 2u, vo1 = vo0 + 32u * LDKV * 2u;
;     ...
;   f32x16 pA0, pA1, pB0, pB1; float mnA, mnB, alA, alB; bf16x8 pa0, pa1, pa2, pa3; const int NT = seq / KVBLK;
;   const char* Kl0 = (const char*)K_lds; const char* Kl1 = (const char*)(K_lds + SHM_K);
;   constexpr int SE = 0, SO = 1;
;   SLOAD(SE, 0); asm volatile("s_waitcnt vmcnt(0)" ::: "memory"); SWRITE(0, SE); __syncthreads();
;   qkt<HALF>(pA0, pA1, Kl0, qr, r32, hi, koff); partialSM(pA0, pA1, m_reg, mnA, alA);
;   SLOAD(SO, KVBLK); if (2 < NT) SLOAD(SE, 2 * KVBLK);
;   SWAIT(); SWRITE(1, SO); __syncthreads();
.LBB0_453:
	s_ashr_i32 s18, s3, 2
	s_add_i32 s3, s3, -8
	s_lshr_b32 s3, s3, 1
	s_add_i32 s3, s3, 2
	s_and_b64 s[6:7], s[14:15], exec
	s_cselect_b32 s3, s18, s3
	s_lshl_b32 s6, s3, 7
	s_cmp_lt_i32 s3, 2
	s_movk_i32 s3, 0x1100
	s_cselect_b32 s3, s3, 0x1500
	s_ashr_i32 s7, s6, 31
	s_add_i32 s18, s3, s6
	s_lshl_b64 s[14:15], s[6:7], 1
	v_cvt_pk_bf16_f32 v98, v30, v20
	v_cvt_pk_bf16_f32 v99, v31, v21
	v_cvt_pk_bf16_f32 v100, v32, v18
	v_cvt_pk_bf16_f32 v101, v33, v19
	v_cvt_pk_bf16_f32 v106, v34, v16
	v_cvt_pk_bf16_f32 v107, v35, v17
	v_ashrrev_i32_e32 v16, 4, v44
	v_lshlrev_b32_e32 v17, 3, v44
	s_movk_i32 s3, 0x300
	s_add_u32 s20, s44, s14
	v_and_b32_e32 v18, 0x78, v17
	v_mul_lo_u32 v0, v16, s3
	s_addc_u32 s21, s45, s15
	s_ashr_i32 s19, s18, 31
	v_or_b32_e32 v0, v0, v18
	s_movk_i32 s3, 0x1800
	s_lshl_b64 s[18:19], s[18:19], 1
	v_lshlrev_b32_e32 v50, 1, v0
	v_mul_lo_u32 v0, v16, s3
	s_add_u32 s22, s30, s18
	v_or_b32_e32 v0, v0, v18
	s_addc_u32 s23, s31, s19
	v_lshlrev_b32_e32 v54, 1, v0
	v_cvt_pk_bf16_f32 v108, v40, v10
	v_cvt_pk_bf16_f32 v109, v41, v11
	v_cvt_pk_bf16_f32 v110, v4, v8
	v_cvt_pk_bf16_f32 v111, v5, v9
	v_cvt_pk_bf16_f32 v112, v2, v36
	v_cvt_pk_bf16_f32 v113, v1, v37
	v_cvt_pk_bf16_f32 v102, v24, v6
	v_cvt_pk_bf16_f32 v103, v23, v7
	v_cvt_pk_bf16_f32 v104, v14, v26
	v_cvt_pk_bf16_f32 v105, v13, v27
	v_add_u32_e32 v48, 0xc000, v50
	v_add_u32_e32 v52, 0x60000, v54
	v_readlane_b32 s52, v252, 4
	s_nop 3
	v_and_b32_e32 v236, 63, v44
	v_lshrrev_b32_e32 v237, 4, v236
	v_and_b32_e32 v238, 15, v236
	s_lshl_b32 s53, s52, 3
	v_add_u32_e32 v239, s53, v237
	v_xor_b32_e32 v240, v238, v237
	v_mul_u32_u24_e32 v232, 0x600, v239
	v_lshl_add_u32 v232, v240, 4, v232
	v_add_u32_e32 v241, 4, v237
	v_xor_b32_e32 v240, v238, v241
	v_add_u32_e32 v239, 4, v239
	v_mul_u32_u24_e32 v233, 0x600, v239
	v_lshl_add_u32 v233, v240, 4, v233
	v_bfe_u32 v237, v236, 2, 3
	v_add_u32_e32 v237, s53, v237
	v_and_b32_e32 v238, 4, v237
	v_and_b32_e32 v239, 8, v237
	v_and_b32_e32 v237, 0xfffffff3, v237
	v_lshl_or_b32 v237, v238, 1, v237
	v_lshrrev_b32_e32 v239, 1, v239
	v_or_b32_e32 v237, v237, v239
	v_mul_u32_u24_e32 v234, 0x3000, v237
	v_lshrrev_b32_e32 v238, 5, v236
	v_lshl_add_u32 v234, v238, 6, v234
	v_and_b32_e32 v238, 3, v236
	v_lshl_add_u32 v234, v238, 4, v234
	v_add_u32_e32 v235, 0x80, v234
	s_lshl_b32 s53, s52, 11
	s_add_i32 s52, s53, 0x8000
	s_add_i32 m0, s52, 0x0
	s_nop 0
	global_load_lds_dwordx4 v232, s[20:21]
	s_add_i32 m0, s52, 0x400
	s_nop 0
	global_load_lds_dwordx4 v233, s[20:21]
	s_add_i32 m0, s53, 0x0
	s_nop 0
	global_load_lds_dwordx4 v234, s[22:23]
	s_add_i32 m0, s53, 0x400
	s_nop 0
	global_load_lds_dwordx4 v235, s[22:23]
	s_add_u32 s48, s20, 0x18000
	s_addc_u32 s49, s21, 0
	s_add_u32 s50, s22, 0xc0000
	s_addc_u32 s51, s23, 0
	s_add_i32 m0, s52, 0x4000
	s_nop 0
	global_load_lds_dwordx4 v232, s[48:49]
	s_add_i32 m0, s52, 0x4400
	s_nop 0
	global_load_lds_dwordx4 v233, s[48:49]
	s_add_i32 m0, s53, 0x4000
	s_nop 0
	global_load_lds_dwordx4 v234, s[50:51]
	s_add_i32 m0, s53, 0x4400
	s_nop 0
	global_load_lds_dwordx4 v235, s[50:51]
	s_add_u32 s48, s48, 0x18000
	s_addc_u32 s49, s49, 0
	s_add_u32 s50, s50, 0xc0000
	s_addc_u32 s51, s51, 0
	v_lshlrev_b32_e32 v20, 4, v180
	v_and_b32_e32 v21, 0xfffff0, v16
	v_lshlrev_b32_e32 v22, 1, v16
	v_lshrrev_b32_e32 v23, 1, v16
	v_and_b32_e32 v24, 3, v16
	v_add_u32_e32 v25, 32, v16
	v_and_b32_e32 v73, 0x70, v20
	v_and_or_b32 v20, v22, 8, v21
	v_and_b32_e32 v19, 0x70, v44
	v_bfe_u32 v17, v17, 5, 2
	v_lshlrev_b32_e32 v16, 8, v16
	v_and_or_b32 v21, v23, 4, v24
	v_lshlrev_b32_e32 v18, 1, v18
	v_and_b32_e32 v22, 0xfffff0, v25
	v_lshlrev_b32_e32 v23, 1, v25
	v_lshlrev_b32_e32 v24, 8, v25
	v_lshrrev_b32_e32 v20, 1, v20
	v_and_b32_e32 v25, 48, v18
	v_and_or_b32 v22, v23, 8, v22
	v_bitop3_b32 v16, v18, v16, v19 bitop3:0xde
	v_bitop3_b32 v18, v18, v24, v19 bitop3:0xde
	v_or_b32_e32 v19, v20, v17
	v_lshlrev_b32_e32 v21, 6, v21
	v_lshrrev_b32_e32 v20, 1, v22
	v_add_u32_e32 v188, 0, v16
	v_lshlrev_b32_e32 v16, 9, v19
	s_and_b32 s3, s17, 0x80
	v_lshlrev_b32_e32 v72, 8, v180
	v_or_b32_e32 v17, v20, v17
	v_or3_b32 v16, v16, v21, v25
	v_or_b32_e32 v74, s3, v96
	v_lshlrev_b32_e32 v17, 9, v17
	v_add_u32_e32 v190, 0, v16
	v_bitop3_b32 v16, v74, v72, v73 bitop3:0xde
	v_or3_b32 v17, v17, v21, v25
	v_add_u32_e32 v192, 0, v16
	v_add_u32_e32 v189, 0, v18
	v_add_u32_e32 v191, 0, v17
	s_waitcnt vmcnt(0)
	v_and_b32_e32 v76, 63, v44
	s_add_u32 s6, s20, 0x18000
	s_addc_u32 s7, s21, 0
	s_add_u32 s38, s22, 0xc0000
	s_addc_u32 s39, s23, 0
	s_mov_b32 s64, s65
	s_waitcnt lgkmcnt(0)
	s_barrier
; #define SWRITE(b, i) do { *(LAS bf16x8*)(V_lds + (b) * SHM_V + vst0) = sr_[i].vs0;          \
;     *(LAS bf16x8*)(V_lds + (b) * SHM_V + vst1) = sr_[i].vs1; int kc = sc * 2;               \
;     *(LAS bf16x8*)(K_lds + (b) * SHM_K + KSWZ(sr, kc)) = sr_[i].ks0;                       \
;     *(LAS bf16x8*)(K_lds + (b) * SHM_K + KSWZ(32 + sr, kc)) = sr_[i].ks1; } while (0)
; #define SWAIT() asm volatile("s_waitcnt vmcnt(4)" ::: "memory")
; __device__ __forceinline__ void partialSM(f32x16& p0, f32x16& p1, float& m_reg, float& mn, float& alpha) {
;   constexpr float C = SCALE * 1.4426950408889634f;
;   float pmax = p0[0]; for (int r = 1; r < 16; ++r) pmax = fmaxf(pmax, p0[r]); for (int r = 0; r < 16; ++r) pmax = fmaxf(pmax, p1[r]);
;   { auto rr = __builtin_amdgcn_permlane32_swap(__float_as_uint(pmax), __float_as_uint(pmax), false, false);
;     pmax = fmaxf(__uint_as_float(rr[0]), __uint_as_float(rr[1])); }
;   if (__builtin_expect(__all(pmax - m_reg <= THR / SCALE), 1)) { mn = m_reg; alpha = 1.f; }
;   else { mn = fmaxf(m_reg, pmax); alpha = __builtin_amdgcn_exp2f((m_reg - mn) * C); m_reg = mn; }
;   float mnC = -mn * C;
;   for (int r = 0; r < 16; ++r) p0[r] = fmaf(p0[r], C, mnC); for (int r = 0; r < 16; ++r) p1[r] = fmaf(p1[r], C, mnC);
;   for (int r = 0; r < 16; ++r) p0[r] = __builtin_amdgcn_exp2f(p0[r]);
; }
; template <bool HALF> __device__ __forceinline__ void qkt(f32x16& p0, f32x16& p1, const char* Ks, const bf16x8* qr, int r32, int hi, int koff) {
;   p0 = f32x16{}; p1 = f32x16{};
;   for (int d0 = 0; d0 < (HALF ? 4 : 8); ++d0) { int cb = (d0 * 16 + hi * 8) * 2 + koff;
;     bf16x8 b0 = *reinterpret_cast<const bf16x8*>(Ks + KSWZ(r32, cb));
;     bf16x8 b1 = *reinterpret_cast<const bf16x8*>(Ks + KSWZ(32 + r32, cb));
;     p0 = __builtin_amdgcn_mfma_f32_32x32x16_bf16(b0, qr[d0], p0, 0, 0, 0);
;     p1 = __builtin_amdgcn_mfma_f32_32x32x16_bf16(b1, qr[d0], p1, 0, 0, 0); }
; template <bool HALF> __device__ __forceinline__ void dense_body(const bf16_t* __restrict__ Qb, const bf16_t* __restrict__ Kh, const bf16_t* __restrict__ Vh, ...
;     ...
;   qkt<HALF>(pA0, pA1, Kl0, qr, r32, hi, koff); partialSM(pA0, pA1, m_reg, mnA, alA);
;   SLOAD(SO, KVBLK); if (2 < NT) SLOAD(SE, 2 * KVBLK);
;   SWAIT(); SWRITE(1, SO); __syncthreads();
	ds_read_b128 v[0:3], v192 offset:32768
	ds_read_b128 v[4:7], v192 offset:40960
	s_waitcnt lgkmcnt(1)
	v_mfma_f32_32x32x16_bf16 v[16:31], v[0:3], v[98:101], 0
	v_and_b32_e32 v0, 0x3fffffc0, v44
	v_lshl_add_u32 v183, v0, 2, s46
	v_lshlrev_b32_e32 v0, 4, v76
	v_lshlrev_b32_e32 v8, 3, v76
	v_and_b32_e32 v0, 0xc0, v0
	v_and_or_b32 v9, v8, 24, v0
	v_or_b32_e32 v0, 32, v74
	v_bitop3_b32 v0, v0, v72, v73 bitop3:0xde
	v_add_u32_e32 v193, 0, v0
	s_waitcnt lgkmcnt(0)
	v_mfma_f32_32x32x16_bf16 v[32:47], v[4:7], v[98:101], 0
	ds_read_b128 v[0:3], v193 offset:32768
	ds_read_b128 v[4:7], v193 offset:40960
	s_add_u32 s6, s20, 0x30000
	s_addc_u32 s7, s21, 0
	v_and_b32_e32 v8, 0x100, v8
	s_mov_b32 s66, s65
	s_mov_b32 s67, s65
	s_waitcnt lgkmcnt(1)
	v_mfma_f32_32x32x16_bf16 v[16:31], v[0:3], v[106:109], v[16:31]
	v_lshlrev_b32_e32 v0, 1, v76
	v_and_b32_e32 v10, 32, v0
	v_or_b32_e32 v0, 64, v74
	v_bitop3_b32 v0, v0, v72, v73 bitop3:0xde
	v_add_u32_e32 v195, 0, v0
	ds_read_b128 v[0:3], v195 offset:32768
	v_or3_b32 v77, v9, v10, v8
	s_waitcnt lgkmcnt(1)
	v_mfma_f32_32x32x16_bf16 v[32:47], v[4:7], v[106:109], v[32:47]
	ds_read_b128 v[4:7], v195 offset:40960
	s_mov_b32 s68, s65
	s_mov_b32 s69, s65
	s_mov_b32 s70, s65
	s_mov_b32 s71, s65
	s_mov_b32 s72, s65
	s_mov_b32 s73, s65
	s_waitcnt lgkmcnt(1)
	v_mfma_f32_32x32x16_bf16 v[16:31], v[0:3], v[110:113], v[16:31]
	v_or_b32_e32 v0, 0x60, v74
	v_bitop3_b32 v0, v0, v72, v73 bitop3:0xde
	v_add_u32_e32 v194, 0, v0
	ds_read_b128 v[0:3], v194 offset:32768
	ds_read_b128 v[72:75], v194 offset:40960
	s_add_u32 s6, s22, 0x180000
	s_addc_u32 s7, s23, 0
	s_waitcnt lgkmcnt(2)
	v_mfma_f32_32x32x16_bf16 v[32:47], v[4:7], v[110:113], v[32:47]
	s_mov_b32 s74, s65
	s_mov_b32 s75, s65
	s_waitcnt lgkmcnt(1)
	v_mfma_f32_32x32x16_bf16 v[16:31], v[0:3], v[102:105], v[16:31]
	s_mov_b32 s76, s65
	s_mov_b32 s77, s65
	s_mov_b32 s78, s65
	s_mov_b32 s79, s65
	v_mov_b64_e32 v[0:1], s[64:65]
	v_mov_b32_e32 v55, v97
	v_mov_b32_e32 v53, v97
	s_waitcnt lgkmcnt(0)
	v_mfma_f32_32x32x16_bf16 v[32:47], v[72:75], v[102:105], v[32:47]
	s_nop 2
	v_max_f32_e32 v72, v17, v17
	v_max_f32_e32 v73, v16, v16
	v_max_f32_e32 v72, v73, v72
	v_max3_f32 v72, v72, v18, v19
	v_max3_f32 v72, v72, v20, v21
	v_max3_f32 v72, v72, v22, v23
	v_max3_f32 v72, v72, v24, v25
	v_max3_f32 v72, v72, v26, v27
	v_max3_f32 v72, v72, v28, v29
	v_max3_f32 v72, v72, v30, v31
	v_max3_f32 v72, v72, v32, v33
	v_max3_f32 v72, v72, v34, v35
	v_max3_f32 v72, v72, v36, v37
	v_max3_f32 v72, v72, v38, v39
	v_max3_f32 v72, v72, v40, v41
	v_max3_f32 v72, v72, v42, v43
	v_max3_f32 v72, v72, v44, v45
	v_max3_f32 v72, v72, v46, v47
	v_mov_b32_e32 v73, v72
	s_nop 1
	v_permlane32_swap_b32_e32 v72, v73
	v_max_f32_e32 v73, v73, v73
	v_max_f32_e32 v72, v72, v72
	v_max_f32_e32 v72, v72, v73
	v_add_f32_e32 v73, 0x7149f2ca, v72
	v_cmp_ge_f32_e32 vcc, s87, v73
	s_cmp_eq_u64 vcc, exec
	v_max_f32_e32 v56, 0xf149f2ca, v72
	s_cselect_b64 vcc, -1, 0
	v_cndmask_b32_e32 v150, v56, v217, vcc
	v_sub_f32_e32 v57, 0xf149f2ca, v56
	v_mul_f32_e32 v56, 0xbe0293ee, v150
	v_fmamk_f32 v16, v16, 0x3e0293ee, v56
	v_exp_f32_e32 v147, v16
	v_fmamk_f32 v16, v17, 0x3e0293ee, v56
	v_exp_f32_e32 v160, v16
	v_fmamk_f32 v16, v18, 0x3e0293ee, v56
	v_exp_f32_e32 v148, v16
	v_fmamk_f32 v16, v19, 0x3e0293ee, v56
	v_exp_f32_e32 v161, v16
	v_fmamk_f32 v16, v20, 0x3e0293ee, v56
	v_exp_f32_e32 v149, v16
	v_fmamk_f32 v16, v21, 0x3e0293ee, v56
	v_exp_f32_e32 v170, v16
	v_fmamk_f32 v16, v22, 0x3e0293ee, v56
	v_exp_f32_e32 v159, v16
	v_fmamk_f32 v16, v23, 0x3e0293ee, v56
	v_exp_f32_e32 v171, v16
	v_fmamk_f32 v16, v24, 0x3e0293ee, v56
	v_mul_f32_e32 v57, 0x3e0293ee, v57
	v_exp_f32_e32 v151, v16
	v_fmamk_f32 v16, v25, 0x3e0293ee, v56
	v_exp_f32_e32 v57, v57
	v_exp_f32_e32 v155, v16
	v_fmamk_f32 v16, v26, 0x3e0293ee, v56
	v_exp_f32_e32 v152, v16
	v_fmamk_f32 v16, v27, 0x3e0293ee, v56
	v_exp_f32_e32 v156, v16
	v_fmamk_f32 v16, v28, 0x3e0293ee, v56
	v_exp_f32_e32 v153, v16
	v_fmamk_f32 v16, v29, 0x3e0293ee, v56
	v_pk_fma_f32 v[130:131], v[46:47], s[10:11], v[56:57] op_sel_hi:[1,0,0]
	v_pk_fma_f32 v[136:137], v[44:45], s[10:11], v[56:57] op_sel_hi:[1,0,0]
	v_pk_fma_f32 v[140:141], v[42:43], s[10:11], v[56:57] op_sel_hi:[1,0,0]
	v_pk_fma_f32 v[132:133], v[40:41], s[10:11], v[56:57] op_sel_hi:[1,0,0]
	v_pk_fma_f32 v[134:135], v[38:39], s[10:11], v[56:57] op_sel_hi:[1,0,0]
	v_pk_fma_f32 v[138:139], v[36:37], s[10:11], v[56:57] op_sel_hi:[1,0,0]
	v_pk_fma_f32 v[142:143], v[34:35], s[10:11], v[56:57] op_sel_hi:[1,0,0]
	v_pk_fma_f32 v[144:145], v[32:33], s[10:11], v[56:57] op_sel_hi:[1,0,0]
	v_exp_f32_e32 v157, v16
	v_fmamk_f32 v16, v30, 0x3e0293ee, v56
	v_fmac_f32_e32 v56, 0x3e0293ee, v31
	v_exp_f32_e32 v154, v16
	v_exp_f32_e32 v158, v56
	v_mov_b32_e32 v51, v97
	v_mov_b32_e32 v49, v97
	v_mov_b64_e32 v[14:15], s[78:79]
	v_mov_b64_e32 v[2:3], s[66:67]
	v_mov_b64_e32 v[4:5], s[68:69]
	v_mov_b64_e32 v[6:7], s[70:71]
	v_mov_b64_e32 v[8:9], s[72:73]
	v_mov_b64_e32 v[10:11], s[74:75]
	v_mov_b64_e32 v[12:13], s[76:77]
	v_cndmask_b32_e64 v197, v57, 1.0, vcc
	v_lshl_add_u64 v[162:163], s[18:19], 0, v[54:55]
	v_lshl_add_u64 v[164:165], s[18:19], 0, v[52:53]
	v_lshl_add_u64 v[166:167], s[14:15], 0, v[50:51]
	v_lshl_add_u64 v[168:169], s[14:15], 0, v[48:49]
	v_mov_b64_e32 v[62:63], v[14:15]
	v_mov_b64_e32 v[46:47], v[14:15]
	v_mov_b64_e32 v[30:31], v[14:15]
	s_mov_b32 s3, 4
	v_add_u32_e32 v187, 0, v77
	v_cmp_gt_u32_e64 s[40:41], 32, v76
	v_lshl_add_u32 v184, v180, 2, v183
	v_add_u32_e32 v186, s34, v77
	v_mov_b32_e32 v185, 0
	v_mov_b64_e32 v[60:61], v[12:13]
	v_mov_b64_e32 v[58:59], v[10:11]
	v_mov_b64_e32 v[56:57], v[8:9]
	v_mov_b64_e32 v[54:55], v[6:7]
	v_mov_b64_e32 v[52:53], v[4:5]
	v_mov_b64_e32 v[50:51], v[2:3]
	v_mov_b64_e32 v[48:49], v[0:1]
	v_mov_b64_e32 v[44:45], v[12:13]
	v_mov_b64_e32 v[42:43], v[10:11]
	v_mov_b64_e32 v[40:41], v[8:9]
	v_mov_b64_e32 v[38:39], v[6:7]
	v_mov_b64_e32 v[36:37], v[4:5]
	v_mov_b64_e32 v[34:35], v[2:3]
	v_mov_b64_e32 v[32:33], v[0:1]
	v_mov_b64_e32 v[28:29], v[12:13]
	v_mov_b64_e32 v[26:27], v[10:11]
	v_mov_b64_e32 v[24:25], v[8:9]
	v_mov_b64_e32 v[22:23], v[6:7]
	v_mov_b64_e32 v[20:21], v[4:5]
	v_mov_b64_e32 v[18:19], v[2:3]
	v_mov_b64_e32 v[16:17], v[0:1]
	v_readlane_b32 s78, v255, 23
	s_waitcnt lgkmcnt(0)
	s_barrier
	v_readlane_b32 s79, v255, 24
	s_add_i32 m0, s52, 0x0
	s_nop 0
	global_load_lds_dwordx4 v232, s[48:49]
	s_add_i32 m0, s52, 0x400
	s_nop 0
	global_load_lds_dwordx4 v233, s[48:49]
	s_add_u32 s48, s48, 0x18000
	s_addc_u32 s49, s49, 0
; #define SBAR() __builtin_amdgcn_sched_barrier(0)
; __device__ __forceinline__ void finishSM(f32x16& p0, f32x16& p1, float alpha, float& l_reg, bf16x8& pa0, bf16x8& pa1, bf16x8& pa2, bf16x8& pa3) {
;   for (int r = 0; r < 16; ++r) p1[r] = __builtin_amdgcn_exp2f(p1[r]);
;   float ps = 0; for (int r = 0; r < 16; ++r) ps += p0[r]; for (int r = 0; r < 16; ++r) ps += p1[r];
;   { auto rr = __builtin_amdgcn_permlane32_swap(__float_as_uint(ps), __float_as_uint(ps), false, false);
;     ps = __uint_as_float(rr[0]) + __uint_as_float(rr[1]); }
;   l_reg = l_reg * alpha + ps;
;     ...
;   PK4(p0, 0, pa0); PK4(p0, 8, pa1); PK4(p1, 0, pa2); PK4(p1, 8, pa3);
;     ...
; }
; template <bool HALF> __device__ __forceinline__ void dense_body(const bf16_t* __restrict__ Qb, const bf16_t* __restrict__ Kh, const bf16_t* __restrict__ Vh, ...
;     ...
;   for (int j = 1; j + 1 < NT; j += 2) {
;     SBAR(); qkt<HALF>(pB0, pB1, Kl1, qr, r32, hi, koff);
;     finishSM(pA0, pA1, alA, l_reg, pa0, pa1, pa2, pa3); SBAR();
;     SLOAD(SO, (j + 2) * KVBLK); SBAR();
;     pv_d0(o, vb0, pa0, pa1, pa2, pa3); partialSM(pB0, pB1, m_reg, mnB, alB);
.LBB0_454:
	ds_read_b128 v[64:67], v192 offset:49152
	ds_read_b128 v[68:71], v192 offset:57344
	v_add_f32_e32 v146, 0, v147
	v_add_f32_e32 v146, v160, v146
	v_add_f32_e32 v146, v148, v146
	s_waitcnt lgkmcnt(1)
	v_mfma_f32_32x32x16_bf16 v[80:95], v[64:67], v[98:101], 0
	v_add_f32_e32 v146, v161, v146
	v_add_f32_e32 v146, v149, v146
	ds_read_b128 v[172:175], v193 offset:49152
	ds_read_b128 v[198:201], v193 offset:57344
	v_add_f32_e32 v146, v170, v146
	v_add_f32_e32 v146, v159, v146
	v_add_f32_e32 v146, v171, v146
	v_add_f32_e32 v146, v151, v146
	s_waitcnt lgkmcnt(2)
	v_mfma_f32_32x32x16_bf16 v[64:79], v[68:71], v[98:101], 0
	v_add_f32_e32 v146, v155, v146
	v_add_f32_e32 v146, v152, v146
	v_add_f32_e32 v146, v156, v146
	v_exp_f32_e32 v144, v144
	v_add_f32_e32 v146, v153, v146
	v_exp_f32_e32 v145, v145
	v_add_f32_e32 v146, v157, v146
	s_waitcnt lgkmcnt(1)
	v_mfma_f32_32x32x16_bf16 v[80:95], v[172:175], v[106:109], v[80:95]
	v_exp_f32_e32 v142, v142
	v_add_f32_e32 v146, v154, v146
	v_exp_f32_e32 v143, v143
	v_add_f32_e32 v146, v158, v146
	v_exp_f32_e32 v138, v138
	v_add_f32_e32 v146, v144, v146
	v_exp_f32_e32 v139, v139
	s_waitcnt lgkmcnt(0)
	v_mfma_f32_32x32x16_bf16 v[64:79], v[198:201], v[106:109], v[64:79]
	ds_read_b128 v[172:175], v195 offset:49152
	ds_read_b128 v[198:201], v195 offset:57344
	v_add_f32_e32 v146, v145, v146
	v_exp_f32_e32 v134, v134
	v_add_f32_e32 v146, v142, v146
	v_exp_f32_e32 v135, v135
	v_add_f32_e32 v146, v143, v146
	v_exp_f32_e32 v132, v132
	s_waitcnt lgkmcnt(1)
	v_mfma_f32_32x32x16_bf16 v[80:95], v[172:175], v[110:113], v[80:95]
	v_add_f32_e32 v146, v138, v146
	v_exp_f32_e32 v133, v133
	v_add_f32_e32 v146, v139, v146
	v_exp_f32_e32 v140, v140
	v_add_f32_e32 v146, v134, v146
	v_exp_f32_e32 v141, v141
	v_add_f32_e32 v146, v135, v146
	s_waitcnt lgkmcnt(0)
	v_mfma_f32_32x32x16_bf16 v[64:79], v[198:201], v[110:113], v[64:79]
	ds_read_b128 v[172:175], v194 offset:49152
	ds_read_b128 v[198:201], v194 offset:57344
	v_exp_f32_e32 v136, v136
	v_add_f32_e32 v146, v132, v146
	v_exp_f32_e32 v137, v137
	v_add_f32_e32 v146, v133, v146
	v_exp_f32_e32 v130, v130
	v_add_f32_e32 v146, v140, v146
	s_waitcnt lgkmcnt(1)
	v_mfma_f32_32x32x16_bf16 v[80:95], v[172:175], v[102:105], v[80:95]
	v_exp_f32_e32 v131, v131
	v_add_f32_e32 v146, v141, v146
	v_add_f32_e32 v146, v136, v146
	v_add_f32_e32 v146, v137, v146
	v_add_f32_e32 v146, v130, v146
	s_waitcnt lgkmcnt(0)
	v_mfma_f32_32x32x16_bf16 v[64:79], v[198:201], v[102:105], v[64:79]
	v_add_f32_e32 v198, v131, v146
	v_mov_b32_e32 v199, v198
	v_cvt_pk_bf16_f32 v146, v147, v160
	v_cvt_pk_bf16_f32 v147, v148, v161
	v_cvt_pk_bf16_f32 v148, v149, v170
	v_cvt_pk_bf16_f32 v149, v159, v171
	v_cvt_pk_bf16_f32 v200, v151, v155
	v_cvt_pk_bf16_f32 v201, v152, v156
	v_cvt_pk_bf16_f32 v202, v153, v157
	s_nop 1
	v_permlane32_swap_b32_e32 v198, v199
	v_permlane32_swap_b32_e32 v146, v148
	v_cvt_pk_bf16_f32 v203, v154, v158
	v_permlane32_swap_b32_e32 v200, v202
	v_cvt_pk_bf16_f32 v152, v144, v145
	v_cvt_pk_bf16_f32 v153, v142, v143
	v_cvt_pk_bf16_f32 v154, v138, v139
	v_cvt_pk_bf16_f32 v155, v134, v135
	v_cvt_pk_bf16_f32 v156, v132, v133
	v_cvt_pk_bf16_f32 v157, v140, v141
	v_cvt_pk_bf16_f32 v158, v136, v137
	v_cvt_pk_bf16_f32 v159, v130, v131
	v_permlane32_swap_b32_e32 v147, v149
	v_permlane32_swap_b32_e32 v201, v203
	v_permlane32_swap_b32_e32 v152, v154
	v_permlane32_swap_b32_e32 v153, v155
	v_permlane32_swap_b32_e32 v156, v158
	v_permlane32_swap_b32_e32 v157, v159
	ds_read_b64_tr_b16 v[204:205], v187 offset:0
	ds_read_b64_tr_b16 v[206:207], v187 offset:0x800
	ds_read_b64_tr_b16 v[208:209], v187 offset:0x1000
	ds_read_b64_tr_b16 v[210:211], v187 offset:0x1800
	ds_read_b64_tr_b16 v[212:213], v187 offset:0x2000
	ds_read_b64_tr_b16 v[214:215], v187 offset:0x2800
	ds_read_b64_tr_b16 v[222:223], v187 offset:0x3000
	ds_read_b64_tr_b16 v[224:225], v187 offset:0x3800
	s_waitcnt lgkmcnt(0)
	s_nop 0
	v_mfma_f32_32x32x16_bf16 v[0:15], v[146:149], v[204:207], v[0:15]
	ds_read_b64_tr_b16 v[204:205], v187 offset:0x200
	ds_read_b64_tr_b16 v[206:207], v187 offset:0xa00
	v_mfma_f32_32x32x16_bf16 v[0:15], v[200:203], v[208:211], v[0:15]
	ds_read_b64_tr_b16 v[208:209], v187 offset:0x1200
	ds_read_b64_tr_b16 v[210:211], v187 offset:0x1a00
	v_mfma_f32_32x32x16_bf16 v[0:15], v[152:155], v[212:215], v[0:15]
	ds_read_b64_tr_b16 v[212:213], v187 offset:0x2200
	ds_read_b64_tr_b16 v[214:215], v187 offset:0x2a00
	v_mfma_f32_32x32x16_bf16 v[0:15], v[156:159], v[222:225], v[0:15]
	ds_read_b64_tr_b16 v[222:223], v187 offset:0x3200
	ds_read_b64_tr_b16 v[224:225], v187 offset:0x3a00
	s_waitcnt lgkmcnt(0)
; #define SWRITE(b, i) do { *(LAS bf16x8*)(V_lds + (b) * SHM_V + vst0) = sr_[i].vs0;          \
;     *(LAS bf16x8*)(V_lds + (b) * SHM_V + vst1) = sr_[i].vs1; int kc = sc * 2;               \
;     *(LAS bf16x8*)(K_lds + (b) * SHM_K + KSWZ(sr, kc)) = sr_[i].ks0;                       \
;     *(LAS bf16x8*)(K_lds + (b) * SHM_K + KSWZ(32 + sr, kc)) = sr_[i].ks1; } while (0)
; #define SWAIT() asm volatile("s_waitcnt vmcnt(4)" ::: "memory")
; #define RESC(a) do { if (__any((a) < 1.f)) { if (hi == 0) al_l[r32] = (a); asm volatile("s_waitcnt lgkmcnt(0)" ::: "memory"); \
;     for (int d = 0; d < 4; ++d) for (int r = 0; r < 16; ++r) o[d][r] *= al_l[crow(r, hi)]; } } while (0)
; __device__ __forceinline__ void partialSM(f32x16& p0, f32x16& p1, float& m_reg, float& mn, float& alpha) {
;   constexpr float C = SCALE * 1.4426950408889634f;
;   float pmax = p0[0]; for (int r = 1; r < 16; ++r) pmax = fmaxf(pmax, p0[r]); for (int r = 0; r < 16; ++r) pmax = fmaxf(pmax, p1[r]);
;   { auto rr = __builtin_amdgcn_permlane32_swap(__float_as_uint(pmax), __float_as_uint(pmax), false, false);
;     pmax = fmaxf(__uint_as_float(rr[0]), __uint_as_float(rr[1])); }
;   if (__builtin_expect(__all(pmax - m_reg <= THR / SCALE), 1)) { mn = m_reg; alpha = 1.f; }
;   else { mn = fmaxf(m_reg, pmax); alpha = __builtin_amdgcn_exp2f((m_reg - mn) * C); m_reg = mn; }
; template <bool HALF> __device__ __forceinline__ void dense_body(const bf16_t* __restrict__ Qb, const bf16_t* __restrict__ Kh, const bf16_t* __restrict__ Vh, ...
;     ...
;     pv_d0(o, vb0, pa0, pa1, pa2, pa3); partialSM(pB0, pB1, m_reg, mnB, alB);
;     __syncthreads(); SWAIT(); SWRITE(0, SE);
;     RESC(alB); __syncthreads();
	v_mfma_f32_32x32x16_bf16 v[48:63], v[146:149], v[204:207], v[48:63]
	ds_read_b64_tr_b16 v[204:205], v187 offset:0x400
	ds_read_b64_tr_b16 v[206:207], v187 offset:0xc00
	v_mfma_f32_32x32x16_bf16 v[48:63], v[200:203], v[208:211], v[48:63]
	ds_read_b64_tr_b16 v[208:209], v187 offset:0x1400
	ds_read_b64_tr_b16 v[210:211], v187 offset:0x1c00
	v_mfma_f32_32x32x16_bf16 v[48:63], v[152:155], v[212:215], v[48:63]
	ds_read_b64_tr_b16 v[212:213], v187 offset:0x2400
	ds_read_b64_tr_b16 v[214:215], v187 offset:0x2c00
	v_mfma_f32_32x32x16_bf16 v[48:63], v[156:159], v[222:225], v[48:63]
	ds_read_b64_tr_b16 v[222:223], v187 offset:0x3400
	ds_read_b64_tr_b16 v[224:225], v187 offset:0x3c00
	s_waitcnt lgkmcnt(0)
	v_mfma_f32_32x32x16_bf16 v[32:47], v[146:149], v[204:207], v[32:47]
	ds_read_b64_tr_b16 v[204:205], v187 offset:0x600
	ds_read_b64_tr_b16 v[206:207], v187 offset:0xe00
	v_mfma_f32_32x32x16_bf16 v[32:47], v[200:203], v[208:211], v[32:47]
	ds_read_b64_tr_b16 v[208:209], v187 offset:0x1600
	ds_read_b64_tr_b16 v[210:211], v187 offset:0x1e00
	v_mfma_f32_32x32x16_bf16 v[32:47], v[152:155], v[212:215], v[32:47]
	ds_read_b64_tr_b16 v[212:213], v187 offset:0x2600
	ds_read_b64_tr_b16 v[214:215], v187 offset:0x2e00
	v_mfma_f32_32x32x16_bf16 v[32:47], v[156:159], v[222:225], v[32:47]
	ds_read_b64_tr_b16 v[222:223], v187 offset:0x3600
	ds_read_b64_tr_b16 v[224:225], v187 offset:0x3e00
	s_waitcnt lgkmcnt(0)
	v_mfma_f32_32x32x16_bf16 v[16:31], v[146:149], v[204:207], v[16:31]
	v_max_f32_e32 v146, v81, v81
	v_max_f32_e32 v147, v80, v80
	v_max_f32_e32 v146, v147, v146
	v_max3_f32 v146, v146, v82, v83
	v_max3_f32 v146, v146, v84, v85
	v_max3_f32 v146, v146, v86, v87
	v_max3_f32 v146, v146, v88, v89
	v_max3_f32 v146, v146, v90, v91
	v_max3_f32 v146, v146, v92, v93
	v_mfma_f32_32x32x16_bf16 v[16:31], v[200:203], v[208:211], v[16:31]
	v_max3_f32 v146, v146, v94, v95
	v_max3_f32 v146, v146, v64, v65
	v_max3_f32 v146, v146, v66, v67
	v_max3_f32 v146, v146, v68, v69
	v_max3_f32 v146, v146, v70, v71
	v_max3_f32 v146, v146, v72, v73
	v_max3_f32 v146, v146, v74, v75
	v_max3_f32 v146, v146, v76, v77
	v_mfma_f32_32x32x16_bf16 v[16:31], v[152:155], v[212:215], v[16:31]
	v_max3_f32 v146, v146, v78, v79
	v_mov_b32_e32 v147, v146
	s_nop 1
	v_permlane32_swap_b32_e32 v146, v147
	v_max_f32_e32 v147, v147, v147
	v_max_f32_e32 v146, v146, v146
	v_max_f32_e32 v146, v146, v147
	v_sub_f32_e32 v147, v146, v150
	v_cmp_ge_f32_e32 vcc, s87, v147
	v_max_f32_e32 v147, v150, v150
	v_max_f32_e32 v146, v147, v146
	v_mfma_f32_32x32x16_bf16 v[16:31], v[156:159], v[222:225], v[16:31]
	v_sub_f32_e32 v147, v150, v146
	v_mul_f32_e32 v147, 0x3e0293ee, v147
	v_exp_f32_e32 v147, v147
	s_cmp_eq_u64 vcc, exec
	s_cselect_b64 s[42:43], -1, 0
	s_barrier
	s_waitcnt vmcnt(0)
	s_add_i32 m0, s52, 0x4000
	s_nop 0
	global_load_lds_dwordx4 v232, s[48:49]
	s_add_i32 m0, s52, 0x4400
	s_nop 0
	global_load_lds_dwordx4 v233, s[48:49]
	s_add_i32 m0, s53, 0x0
	s_nop 0
	global_load_lds_dwordx4 v234, s[50:51]
	s_add_i32 m0, s53, 0x400
	s_nop 0
	global_load_lds_dwordx4 v235, s[50:51]
	s_add_u32 s48, s48, 0x18000
	s_addc_u32 s49, s49, 0
	s_add_u32 s50, s50, 0xc0000
	s_addc_u32 s51, s51, 0
	v_cndmask_b32_e64 v200, v147, 1.0, s[42:43]
	v_cmp_gt_f32_e32 vcc, 1.0, v200
	s_cbranch_vccz .LBB0_458
	s_and_saveexec_b64 s[6:7], s[40:41]
	ds_write_b32 v184, v200 offset:128
	s_or_b64 exec, exec, s[6:7]
	s_waitcnt lgkmcnt(0)
	v_add_u32_e32 v147, v183, v96
	ds_read_b128 v[152:155], v147 offset:224
	ds_read_b128 v[156:159], v147 offset:192
	ds_read_b128 v[202:205], v147 offset:160
	ds_read_b128 v[206:209], v147 offset:128
	s_waitcnt lgkmcnt(3)
	v_pk_mul_f32 v[12:13], v[12:13], v[152:153]
	s_waitcnt lgkmcnt(2)
	v_pk_mul_f32 v[8:9], v[8:9], v[156:157]
	s_waitcnt lgkmcnt(1)
	v_pk_mul_f32 v[4:5], v[4:5], v[202:203]
	v_pk_mul_f32 v[14:15], v[14:15], v[154:155]
	v_pk_mul_f32 v[10:11], v[10:11], v[158:159]
	v_pk_mul_f32 v[6:7], v[6:7], v[204:205]
	s_waitcnt lgkmcnt(0)
	v_pk_mul_f32 v[2:3], v[2:3], v[208:209]
	v_pk_mul_f32 v[0:1], v[0:1], v[206:207]
	v_pk_mul_f32 v[60:61], v[60:61], v[152:153]
	v_pk_mul_f32 v[56:57], v[56:57], v[156:157]
	v_pk_mul_f32 v[52:53], v[52:53], v[202:203]
	v_pk_mul_f32 v[62:63], v[62:63], v[154:155]
	v_pk_mul_f32 v[58:59], v[58:59], v[158:159]
	v_pk_mul_f32 v[54:55], v[54:55], v[204:205]
	v_pk_mul_f32 v[50:51], v[50:51], v[208:209]
	v_pk_mul_f32 v[48:49], v[48:49], v[206:207]
	v_pk_mul_f32 v[44:45], v[44:45], v[152:153]
	v_pk_mul_f32 v[40:41], v[40:41], v[156:157]
	v_pk_mul_f32 v[36:37], v[36:37], v[202:203]
	v_pk_mul_f32 v[46:47], v[46:47], v[154:155]
	v_pk_mul_f32 v[42:43], v[42:43], v[158:159]
	v_pk_mul_f32 v[38:39], v[38:39], v[204:205]
	v_pk_mul_f32 v[34:35], v[34:35], v[208:209]
	v_pk_mul_f32 v[32:33], v[32:33], v[206:207]
	v_pk_mul_f32 v[28:29], v[28:29], v[152:153]
	v_pk_mul_f32 v[24:25], v[24:25], v[156:157]
	v_pk_mul_f32 v[20:21], v[20:21], v[202:203]
	v_pk_mul_f32 v[30:31], v[30:31], v[154:155]
	v_pk_mul_f32 v[26:27], v[26:27], v[158:159]
	v_pk_mul_f32 v[22:23], v[22:23], v[204:205]
	v_pk_mul_f32 v[18:19], v[18:19], v[208:209]
	v_pk_mul_f32 v[16:17], v[16:17], v[206:207]

; #define SBAR() __builtin_amdgcn_sched_barrier(0)
; #define SWRITE(b, i) do { *(LAS bf16x8*)(V_lds + (b) * SHM_V + vst0) = sr_[i].vs0;          \
;     *(LAS bf16x8*)(V_lds + (b) * SHM_V + vst1) = sr_[i].vs1; int kc = sc * 2;               \
;     *(LAS bf16x8*)(K_lds + (b) * SHM_K + KSWZ(sr, kc)) = sr_[i].ks0;                       \
;     *(LAS bf16x8*)(K_lds + (b) * SHM_K + KSWZ(32 + sr, kc)) = sr_[i].ks1; } while (0)
; #define SWAIT() asm volatile("s_waitcnt vmcnt(4)" ::: "memory")
; #define RESC(a) do { if (__any((a) < 1.f)) { if (hi == 0) al_l[r32] = (a); asm volatile("s_waitcnt lgkmcnt(0)" ::: "memory"); \
;     for (int d = 0; d < 4; ++d) for (int r = 0; r < 16; ++r) o[d][r] *= al_l[crow(r, hi)]; } } while (0)
; __device__ __forceinline__ void partialSM(f32x16& p0, f32x16& p1, float& m_reg, float& mn, float& alpha) {
;   constexpr float C = SCALE * 1.4426950408889634f;
;   float pmax = p0[0]; for (int r = 1; r < 16; ++r) pmax = fmaxf(pmax, p0[r]); for (int r = 0; r < 16; ++r) pmax = fmaxf(pmax, p1[r]);
;   { auto rr = __builtin_amdgcn_permlane32_swap(__float_as_uint(pmax), __float_as_uint(pmax), false, false);
;     pmax = fmaxf(__uint_as_float(rr[0]), __uint_as_float(rr[1])); }
;   if (__builtin_expect(__all(pmax - m_reg <= THR / SCALE), 1)) { mn = m_reg; alpha = 1.f; }
;   else { mn = fmaxf(m_reg, pmax); alpha = __builtin_amdgcn_exp2f((m_reg - mn) * C); m_reg = mn; }
; template <bool HALF> __device__ __forceinline__ void dense_body(const bf16_t* __restrict__ Qb, const bf16_t* __restrict__ Kh, const bf16_t* __restrict__ Vh, ...
;     ...
;     if (j + 3 < NT) SLOAD(SE, (j + 3) * KVBLK); SBAR();
;     pv_d0(o, vb0 + (int)SHM_V, pa0, pa1, pa2, pa3); partialSM(pA0, pA1, m_reg, mnA, alA);
;     __syncthreads(); SWAIT(); SWRITE(1, SO);
;     RESC(alA); __syncthreads();
.LBB0_460:
	ds_read_b64_tr_b16 v[170:171], v186 offset:0
	ds_read_b64_tr_b16 v[172:173], v186 offset:0x800
	ds_read_b64_tr_b16 v[174:175], v186 offset:0x1000
	ds_read_b64_tr_b16 v[176:177], v186 offset:0x1800
	ds_read_b64_tr_b16 v[204:205], v186 offset:0x2000
	ds_read_b64_tr_b16 v[206:207], v186 offset:0x2800
	ds_read_b64_tr_b16 v[208:209], v186 offset:0x3000
	ds_read_b64_tr_b16 v[210:211], v186 offset:0x3800
	s_waitcnt lgkmcnt(0)
	s_nop 0
	v_mfma_f32_32x32x16_bf16 v[0:15], v[146:149], v[170:173], v[0:15]
	ds_read_b64_tr_b16 v[170:171], v186 offset:0x200
	ds_read_b64_tr_b16 v[172:173], v186 offset:0xa00
	v_mfma_f32_32x32x16_bf16 v[0:15], v[150:153], v[174:177], v[0:15]
	ds_read_b64_tr_b16 v[174:175], v186 offset:0x1200
	ds_read_b64_tr_b16 v[176:177], v186 offset:0x1a00
	v_mfma_f32_32x32x16_bf16 v[0:15], v[154:157], v[204:207], v[0:15]
	ds_read_b64_tr_b16 v[204:205], v186 offset:0x2200
	ds_read_b64_tr_b16 v[206:207], v186 offset:0x2a00
	v_mfma_f32_32x32x16_bf16 v[0:15], v[158:161], v[208:211], v[0:15]
	ds_read_b64_tr_b16 v[208:209], v186 offset:0x3200
	ds_read_b64_tr_b16 v[210:211], v186 offset:0x3a00
	s_waitcnt lgkmcnt(0)
	v_mfma_f32_32x32x16_bf16 v[48:63], v[146:149], v[170:173], v[48:63]
	ds_read_b64_tr_b16 v[170:171], v186 offset:0x400
	ds_read_b64_tr_b16 v[172:173], v186 offset:0xc00
	v_mfma_f32_32x32x16_bf16 v[48:63], v[150:153], v[174:177], v[48:63]
	ds_read_b64_tr_b16 v[174:175], v186 offset:0x1400
	ds_read_b64_tr_b16 v[176:177], v186 offset:0x1c00
	v_mfma_f32_32x32x16_bf16 v[48:63], v[154:157], v[204:207], v[48:63]
	ds_read_b64_tr_b16 v[204:205], v186 offset:0x2400
	ds_read_b64_tr_b16 v[206:207], v186 offset:0x2c00
	v_mfma_f32_32x32x16_bf16 v[48:63], v[158:161], v[208:211], v[48:63]
	ds_read_b64_tr_b16 v[208:209], v186 offset:0x3400
	ds_read_b64_tr_b16 v[210:211], v186 offset:0x3c00
	s_waitcnt lgkmcnt(0)
	v_mfma_f32_32x32x16_bf16 v[32:47], v[146:149], v[170:173], v[32:47]
	ds_read_b64_tr_b16 v[170:171], v186 offset:0x600
	ds_read_b64_tr_b16 v[172:173], v186 offset:0xe00
	v_mfma_f32_32x32x16_bf16 v[32:47], v[150:153], v[174:177], v[32:47]
	ds_read_b64_tr_b16 v[174:175], v186 offset:0x1600
	ds_read_b64_tr_b16 v[176:177], v186 offset:0x1e00
	v_mfma_f32_32x32x16_bf16 v[32:47], v[154:157], v[204:207], v[32:47]
	ds_read_b64_tr_b16 v[204:205], v186 offset:0x2600
	ds_read_b64_tr_b16 v[206:207], v186 offset:0x2e00
	v_mfma_f32_32x32x16_bf16 v[32:47], v[158:161], v[208:211], v[32:47]
	ds_read_b64_tr_b16 v[208:209], v186 offset:0x3600
	ds_read_b64_tr_b16 v[210:211], v186 offset:0x3e00
	s_waitcnt lgkmcnt(0)
	v_mfma_f32_32x32x16_bf16 v[16:31], v[146:149], v[170:173], v[16:31]
	v_max_f32_e32 v146, v81, v81
	v_max_f32_e32 v147, v80, v80
	v_max_f32_e32 v146, v147, v146
	v_max3_f32 v146, v146, v82, v83
	v_max3_f32 v146, v146, v84, v85
	v_max3_f32 v146, v146, v86, v87
	v_max3_f32 v146, v146, v88, v89
	v_max3_f32 v146, v146, v90, v91
	v_max3_f32 v146, v146, v92, v93
	v_mfma_f32_32x32x16_bf16 v[16:31], v[150:153], v[174:177], v[16:31]
	v_max3_f32 v146, v146, v94, v95
	v_max3_f32 v146, v146, v64, v65
	v_max3_f32 v146, v146, v66, v67
	v_max3_f32 v146, v146, v68, v69
	v_max3_f32 v146, v146, v70, v71
	v_max3_f32 v146, v146, v72, v73
	v_max3_f32 v146, v146, v74, v75
	v_max3_f32 v146, v146, v76, v77
	v_mfma_f32_32x32x16_bf16 v[16:31], v[154:157], v[204:207], v[16:31]
	v_max3_f32 v146, v146, v78, v79
	v_mov_b32_e32 v147, v146
	s_nop 1
	v_permlane32_swap_b32_e32 v146, v147
	v_max_f32_e32 v147, v147, v147
	v_max_f32_e32 v146, v146, v146
	v_max_f32_e32 v146, v146, v147
	v_sub_f32_e32 v147, v146, v201
	v_cmp_ge_f32_e32 vcc, s87, v147
	v_max_f32_e32 v147, v201, v201
	v_max_f32_e32 v147, v147, v146
	v_mfma_f32_32x32x16_bf16 v[16:31], v[158:161], v[208:211], v[16:31]
	v_sub_f32_e32 v146, v201, v147
	v_mul_f32_e32 v146, 0x3e0293ee, v146
	v_exp_f32_e32 v146, v146
	s_cmp_eq_u64 vcc, exec
	s_cselect_b64 s[42:43], -1, 0
	s_barrier
	s_waitcnt vmcnt(0)
	s_add_i32 m0, s52, 0x0
	s_nop 0
	global_load_lds_dwordx4 v232, s[48:49]
	s_add_i32 m0, s52, 0x400
	s_nop 0
	global_load_lds_dwordx4 v233, s[48:49]
	s_add_i32 m0, s53, 0x4000
	s_nop 0
	global_load_lds_dwordx4 v234, s[50:51]
	s_add_i32 m0, s53, 0x4400
	s_nop 0
	global_load_lds_dwordx4 v235, s[50:51]
	s_add_u32 s48, s48, 0x18000
	s_addc_u32 s49, s49, 0
	s_add_u32 s50, s50, 0xc0000
	s_addc_u32 s51, s51, 0
	v_cndmask_b32_e64 v146, v146, 1.0, s[42:43]
	v_cmp_gt_f32_e32 vcc, 1.0, v146
	s_cbranch_vccz .LBB0_464
	s_and_saveexec_b64 s[6:7], s[40:41]
	ds_write_b32 v184, v146 offset:128
	s_or_b64 exec, exec, s[6:7]
	s_waitcnt lgkmcnt(0)
	v_add_u32_e32 v142, v183, v96
	ds_read_b128 v[130:133], v142 offset:224
	ds_read_b128 v[134:137], v142 offset:192
	ds_read_b128 v[138:141], v142 offset:160
	ds_read_b128 v[142:145], v142 offset:128
	s_waitcnt lgkmcnt(3)
	v_pk_mul_f32 v[12:13], v[12:13], v[130:131]
	s_waitcnt lgkmcnt(2)
	v_pk_mul_f32 v[8:9], v[8:9], v[134:135]
	s_waitcnt lgkmcnt(1)
	v_pk_mul_f32 v[4:5], v[4:5], v[138:139]
	v_pk_mul_f32 v[14:15], v[14:15], v[132:133]
	v_pk_mul_f32 v[10:11], v[10:11], v[136:137]
	v_pk_mul_f32 v[6:7], v[6:7], v[140:141]
	s_waitcnt lgkmcnt(0)
	v_pk_mul_f32 v[2:3], v[2:3], v[144:145]
	v_pk_mul_f32 v[0:1], v[0:1], v[142:143]
	v_pk_mul_f32 v[60:61], v[60:61], v[130:131]
	v_pk_mul_f32 v[56:57], v[56:57], v[134:135]
	v_pk_mul_f32 v[52:53], v[52:53], v[138:139]
	v_pk_mul_f32 v[62:63], v[62:63], v[132:133]
	v_pk_mul_f32 v[58:59], v[58:59], v[136:137]
	v_pk_mul_f32 v[54:55], v[54:55], v[140:141]
	v_pk_mul_f32 v[50:51], v[50:51], v[144:145]
	v_pk_mul_f32 v[48:49], v[48:49], v[142:143]
	v_pk_mul_f32 v[44:45], v[44:45], v[130:131]
	v_pk_mul_f32 v[40:41], v[40:41], v[134:135]
	v_pk_mul_f32 v[36:37], v[36:37], v[138:139]
	v_pk_mul_f32 v[46:47], v[46:47], v[132:133]
	v_pk_mul_f32 v[42:43], v[42:43], v[136:137]
	v_pk_mul_f32 v[38:39], v[38:39], v[140:141]
	v_pk_mul_f32 v[34:35], v[34:35], v[144:145]
	v_pk_mul_f32 v[32:33], v[32:33], v[142:143]
	v_pk_mul_f32 v[28:29], v[28:29], v[130:131]
	v_pk_mul_f32 v[24:25], v[24:25], v[134:135]
	v_pk_mul_f32 v[20:21], v[20:21], v[138:139]
	v_pk_mul_f32 v[30:31], v[30:31], v[132:133]
	v_pk_mul_f32 v[26:27], v[26:27], v[136:137]
	v_pk_mul_f32 v[22:23], v[22:23], v[140:141]
	v_pk_mul_f32 v[18:19], v[18:19], v[144:145]
	v_pk_mul_f32 v[16:17], v[16:17], v[142:143]
; #define SBAR() __builtin_amdgcn_sched_barrier(0)
; __device__ __forceinline__ void partialSM(f32x16& p0, f32x16& p1, float& m_reg, float& mn, float& alpha) {
;     ...
;   else { mn = fmaxf(m_reg, pmax); alpha = __builtin_amdgcn_exp2f((m_reg - mn) * C); m_reg = mn; }
;   float mnC = -mn * C;
;   for (int r = 0; r < 16; ++r) p0[r] = fmaf(p0[r], C, mnC); for (int r = 0; r < 16; ++r) p1[r] = fmaf(p1[r], C, mnC);
;   for (int r = 0; r < 16; ++r) p0[r] = __builtin_amdgcn_exp2f(p0[r]);
; }
; __device__ __forceinline__ void finishSM(f32x16& p0, f32x16& p1, float alpha, float& l_reg, bf16x8& pa0, bf16x8& pa1, bf16x8& pa2, bf16x8& pa3) {
;   for (int r = 0; r < 16; ++r) p1[r] = __builtin_amdgcn_exp2f(p1[r]);
;   float ps = 0; for (int r = 0; r < 16; ++r) ps += p0[r]; for (int r = 0; r < 16; ++r) ps += p1[r];
;   { auto rr = __builtin_amdgcn_permlane32_swap(__float_as_uint(ps), __float_as_uint(ps), false, false);
;     ps = __uint_as_float(rr[0]) + __uint_as_float(rr[1]); }
;   l_reg = l_reg * alpha + ps;
;     ...
;   PK4(p0, 0, pa0); PK4(p0, 8, pa1); PK4(p1, 0, pa2); PK4(p1, 8, pa3);
;     ...
; }
; template <bool HALF> __device__ __forceinline__ void dense_body(const bf16_t* __restrict__ Qb, const bf16_t* __restrict__ Kh, const bf16_t* __restrict__ Vh, ...
;     ...
;   SBAR(); qkt<HALF>(pB0, pB1, Kl1, qr, r32, hi, koff);
;   finishSM(pA0, pA1, alA, l_reg, pa0, pa1, pa2, pa3); SBAR();
;   pv_d0(o, vb0, pa0, pa1, pa2, pa3); partialSM(pB0, pB1, m_reg, mnB, alB);
.LBB0_464:
	v_cndmask_b32_e64 v150, v147, v201, s[42:43]
	v_mul_f32_e32 v130, 0xbe0293ee, v150
	v_mov_b32_e32 v131, v130
	v_fmamk_f32 v80, v80, 0x3e0293ee, v130
	v_fmamk_f32 v81, v81, 0x3e0293ee, v130
	v_fmamk_f32 v82, v82, 0x3e0293ee, v130
	v_fmamk_f32 v83, v83, 0x3e0293ee, v130
	v_fmamk_f32 v84, v84, 0x3e0293ee, v130
	v_fmamk_f32 v85, v85, 0x3e0293ee, v130
	v_fmamk_f32 v86, v86, 0x3e0293ee, v130
	v_fmamk_f32 v87, v87, 0x3e0293ee, v130
	v_fmamk_f32 v88, v88, 0x3e0293ee, v130
	v_fmamk_f32 v89, v89, 0x3e0293ee, v130
	v_fmamk_f32 v90, v90, 0x3e0293ee, v130
	v_fmamk_f32 v91, v91, 0x3e0293ee, v130
	v_fmamk_f32 v92, v92, 0x3e0293ee, v130
	v_fmamk_f32 v93, v93, 0x3e0293ee, v130
	v_fmamk_f32 v94, v94, 0x3e0293ee, v130
	v_fmac_f32_e32 v131, 0x3e0293ee, v95
	v_exp_f32_e32 v147, v80
	v_exp_f32_e32 v160, v81
	v_exp_f32_e32 v148, v82
	v_exp_f32_e32 v161, v83
	v_exp_f32_e32 v149, v84
	v_exp_f32_e32 v170, v85
	v_exp_f32_e32 v159, v86
	v_exp_f32_e32 v171, v87
	v_exp_f32_e32 v151, v88
	v_exp_f32_e32 v155, v89
	v_exp_f32_e32 v152, v90
	v_exp_f32_e32 v156, v91
	v_exp_f32_e32 v153, v92
	v_exp_f32_e32 v157, v93
	v_exp_f32_e32 v154, v94
	v_exp_f32_e32 v158, v131
	v_pk_fma_f32 v[144:145], v[64:65], s[10:11], v[130:131] op_sel_hi:[1,0,0]
	v_add_f32_e32 v64, v198, v199
	v_fmac_f32_e32 v64, v197, v185
	v_add_f32_e32 v185, v202, v203
	v_pk_fma_f32 v[142:143], v[66:67], s[10:11], v[130:131] op_sel_hi:[1,0,0]
	v_pk_fma_f32 v[138:139], v[68:69], s[10:11], v[130:131] op_sel_hi:[1,0,0]
	v_pk_fma_f32 v[134:135], v[70:71], s[10:11], v[130:131] op_sel_hi:[1,0,0]
	v_pk_fma_f32 v[132:133], v[72:73], s[10:11], v[130:131] op_sel_hi:[1,0,0]
	v_pk_fma_f32 v[140:141], v[74:75], s[10:11], v[130:131] op_sel_hi:[1,0,0]
	v_pk_fma_f32 v[136:137], v[76:77], s[10:11], v[130:131] op_sel_hi:[1,0,0]
	v_pk_fma_f32 v[130:131], v[78:79], s[10:11], v[130:131] op_sel_hi:[1,0,0]
	v_fmac_f32_e32 v185, v64, v200
	s_add_i32 s3, s3, 2
	s_and_b64 vcc, exec, s[14:15]
	s_waitcnt lgkmcnt(0)
	s_barrier
	s_cbranch_vccnz .LBB0_466
	v_mov_b32_e32 v197, v146
	s_branch .LBB0_454
.LBB0_466:
	ds_read_b128 v[64:67], v192 offset:49152
	ds_read_b128 v[68:71], v192 offset:57344
	v_exp_f32_e32 v118, v140
	v_exp_f32_e32 v119, v141
	v_exp_f32_e32 v120, v136
	s_waitcnt lgkmcnt(1)
	v_mfma_f32_32x32x16_bf16 v[80:95], v[64:67], v[98:101], 0
	v_exp_f32_e32 v121, v137
	v_exp_f32_e32 v122, v130
	v_exp_f32_e32 v123, v131
	s_waitcnt lgkmcnt(0)
	v_mfma_f32_32x32x16_bf16 v[64:79], v[68:71], v[98:101], 0
	ds_read_b128 v[98:101], v193 offset:49152
	ds_read_b128 v[114:117], v193 offset:57344
	s_waitcnt lgkmcnt(1)
	v_mfma_f32_32x32x16_bf16 v[80:95], v[98:101], v[106:109], v[80:95]
	s_waitcnt lgkmcnt(0)
	v_mfma_f32_32x32x16_bf16 v[64:79], v[114:117], v[106:109], v[64:79]
	ds_read_b128 v[98:101], v195 offset:49152
	ds_read_b128 v[106:109], v195 offset:57344
	v_exp_f32_e32 v114, v134
	v_exp_f32_e32 v115, v135
	v_exp_f32_e32 v116, v132
	v_exp_f32_e32 v117, v133
	s_waitcnt lgkmcnt(1)
	v_mfma_f32_32x32x16_bf16 v[80:95], v[98:101], v[110:113], v[80:95]
	s_waitcnt lgkmcnt(0)
	v_mfma_f32_32x32x16_bf16 v[64:79], v[106:109], v[110:113], v[64:79]
	ds_read_b128 v[98:101], v194 offset:49152
	ds_read_b128 v[106:109], v194 offset:57344
	v_exp_f32_e32 v110, v142
	v_exp_f32_e32 v111, v143
	v_exp_f32_e32 v112, v138
	v_exp_f32_e32 v113, v139
	s_waitcnt lgkmcnt(1)
	v_mfma_f32_32x32x16_bf16 v[80:95], v[98:101], v[102:105], v[80:95]
	v_add_f32_e32 v98, 0, v147
	v_add_f32_e32 v98, v160, v98
	v_add_f32_e32 v98, v148, v98
	v_add_f32_e32 v98, v161, v98
	v_add_f32_e32 v98, v149, v98
	v_add_f32_e32 v98, v170, v98
	v_add_f32_e32 v98, v159, v98
	v_add_f32_e32 v98, v171, v98
	v_add_f32_e32 v98, v151, v98
	v_add_f32_e32 v98, v155, v98
	v_add_f32_e32 v98, v152, v98
	v_add_f32_e32 v98, v156, v98
	s_waitcnt lgkmcnt(0)
	v_mfma_f32_32x32x16_bf16 v[64:79], v[106:109], v[102:105], v[64:79]
	v_exp_f32_e32 v108, v144
	v_add_f32_e32 v98, v153, v98
	v_exp_f32_e32 v109, v145
	v_add_f32_e32 v98, v157, v98
	v_add_f32_e32 v98, v154, v98
	v_add_f32_e32 v98, v158, v98
	v_add_f32_e32 v98, v108, v98
	v_add_f32_e32 v98, v109, v98
	v_add_f32_e32 v98, v110, v98
	v_add_f32_e32 v98, v111, v98
	v_add_f32_e32 v98, v112, v98
	v_add_f32_e32 v98, v113, v98
	v_add_f32_e32 v98, v114, v98
	v_add_f32_e32 v98, v115, v98
	v_add_f32_e32 v98, v116, v98
	v_add_f32_e32 v98, v117, v98
	v_add_f32_e32 v98, v118, v98
	v_add_f32_e32 v98, v119, v98
	v_add_f32_e32 v98, v120, v98
	v_add_f32_e32 v98, v121, v98
	v_add_f32_e32 v98, v122, v98
	v_add_f32_e32 v98, v123, v98
	v_mov_b32_e32 v99, v98
	v_cvt_pk_bf16_f32 v100, v147, v160
	v_cvt_pk_bf16_f32 v101, v148, v161
	v_cvt_pk_bf16_f32 v102, v149, v170
	v_cvt_pk_bf16_f32 v103, v159, v171
	s_nop 1
	v_permlane32_swap_b32_e32 v98, v99
	v_permlane32_swap_b32_e32 v100, v102
	v_permlane32_swap_b32_e32 v101, v103
	v_cvt_pk_bf16_f32 v104, v151, v155
	v_cvt_pk_bf16_f32 v105, v152, v156
	v_cvt_pk_bf16_f32 v106, v153, v157
	v_cvt_pk_bf16_f32 v107, v154, v158
	v_cvt_pk_bf16_f32 v108, v108, v109
	v_cvt_pk_bf16_f32 v109, v110, v111
	v_cvt_pk_bf16_f32 v110, v112, v113
	v_cvt_pk_bf16_f32 v111, v114, v115
	v_cvt_pk_bf16_f32 v112, v116, v117
	v_cvt_pk_bf16_f32 v113, v118, v119
	v_cvt_pk_bf16_f32 v114, v120, v121
	v_cvt_pk_bf16_f32 v115, v122, v123
	s_nop 0
	v_permlane32_swap_b32_e32 v104, v106
	v_permlane32_swap_b32_e32 v105, v107
	v_permlane32_swap_b32_e32 v108, v110
	v_permlane32_swap_b32_e32 v109, v111
	v_permlane32_swap_b32_e32 v112, v114
	v_permlane32_swap_b32_e32 v113, v115
	ds_read_b64_tr_b16 v[116:117], v187 offset:0
	ds_read_b64_tr_b16 v[118:119], v187 offset:0x800
	ds_read_b64_tr_b16 v[120:121], v187 offset:0x1000
	ds_read_b64_tr_b16 v[122:123], v187 offset:0x1800
	ds_read_b64_tr_b16 v[124:125], v187 offset:0x2000
	ds_read_b64_tr_b16 v[126:127], v187 offset:0x2800
	ds_read_b64_tr_b16 v[128:129], v187 offset:0x3000
	ds_read_b64_tr_b16 v[130:131], v187 offset:0x3800
	s_waitcnt lgkmcnt(0)
; #define RESC(a) do { if (__any((a) < 1.f)) { if (hi == 0) al_l[r32] = (a); asm volatile("s_waitcnt lgkmcnt(0)" ::: "memory"); \
;     for (int d = 0; d < 4; ++d) for (int r = 0; r < 16; ++r) o[d][r] *= al_l[crow(r, hi)]; } } while (0)
; __device__ __forceinline__ void partialSM(f32x16& p0, f32x16& p1, float& m_reg, float& mn, float& alpha) {
;   constexpr float C = SCALE * 1.4426950408889634f;
;   float pmax = p0[0]; for (int r = 1; r < 16; ++r) pmax = fmaxf(pmax, p0[r]); for (int r = 0; r < 16; ++r) pmax = fmaxf(pmax, p1[r]);
;   { auto rr = __builtin_amdgcn_permlane32_swap(__float_as_uint(pmax), __float_as_uint(pmax), false, false);
;     pmax = fmaxf(__uint_as_float(rr[0]), __uint_as_float(rr[1])); }
;   if (__builtin_expect(__all(pmax - m_reg <= THR / SCALE), 1)) { mn = m_reg; alpha = 1.f; }
;   else { mn = fmaxf(m_reg, pmax); alpha = __builtin_amdgcn_exp2f((m_reg - mn) * C); m_reg = mn; }
; template <bool HALF> __device__ __forceinline__ void dense_body(const bf16_t* __restrict__ Qb, const bf16_t* __restrict__ Kh, const bf16_t* __restrict__ Vh, ...
;     ...
;   pv_d0(o, vb0, pa0, pa1, pa2, pa3); partialSM(pB0, pB1, m_reg, mnB, alB);
;   __syncthreads(); RESC(alB);
	s_nop 0
	v_mfma_f32_32x32x16_bf16 v[0:15], v[100:103], v[116:119], v[0:15]
	ds_read_b64_tr_b16 v[116:117], v187 offset:0x200
	ds_read_b64_tr_b16 v[118:119], v187 offset:0xa00
	v_mfma_f32_32x32x16_bf16 v[0:15], v[104:107], v[120:123], v[0:15]
	ds_read_b64_tr_b16 v[120:121], v187 offset:0x1200
	ds_read_b64_tr_b16 v[122:123], v187 offset:0x1a00
	v_mfma_f32_32x32x16_bf16 v[0:15], v[108:111], v[124:127], v[0:15]
	ds_read_b64_tr_b16 v[124:125], v187 offset:0x2200
	ds_read_b64_tr_b16 v[126:127], v187 offset:0x2a00
	v_mfma_f32_32x32x16_bf16 v[0:15], v[112:115], v[128:131], v[0:15]
	ds_read_b64_tr_b16 v[128:129], v187 offset:0x3200
	ds_read_b64_tr_b16 v[130:131], v187 offset:0x3a00
	s_waitcnt lgkmcnt(0)
	v_mfma_f32_32x32x16_bf16 v[48:63], v[100:103], v[116:119], v[48:63]
	ds_read_b64_tr_b16 v[116:117], v187 offset:0x400
	ds_read_b64_tr_b16 v[118:119], v187 offset:0xc00
	v_mfma_f32_32x32x16_bf16 v[48:63], v[104:107], v[120:123], v[48:63]
	ds_read_b64_tr_b16 v[120:121], v187 offset:0x1400
	ds_read_b64_tr_b16 v[122:123], v187 offset:0x1c00
	v_mfma_f32_32x32x16_bf16 v[48:63], v[108:111], v[124:127], v[48:63]
	ds_read_b64_tr_b16 v[124:125], v187 offset:0x2400
	ds_read_b64_tr_b16 v[126:127], v187 offset:0x2c00
	v_mfma_f32_32x32x16_bf16 v[48:63], v[112:115], v[128:131], v[48:63]
	ds_read_b64_tr_b16 v[128:129], v187 offset:0x3400
	ds_read_b64_tr_b16 v[130:131], v187 offset:0x3c00
	s_waitcnt lgkmcnt(0)
	v_mfma_f32_32x32x16_bf16 v[32:47], v[100:103], v[116:119], v[32:47]
	ds_read_b64_tr_b16 v[116:117], v187 offset:0x600
	ds_read_b64_tr_b16 v[118:119], v187 offset:0xe00
	v_mfma_f32_32x32x16_bf16 v[32:47], v[104:107], v[120:123], v[32:47]
	ds_read_b64_tr_b16 v[120:121], v187 offset:0x1600
	ds_read_b64_tr_b16 v[122:123], v187 offset:0x1e00
	v_mfma_f32_32x32x16_bf16 v[32:47], v[108:111], v[124:127], v[32:47]
	ds_read_b64_tr_b16 v[124:125], v187 offset:0x2600
	ds_read_b64_tr_b16 v[126:127], v187 offset:0x2e00
	v_mfma_f32_32x32x16_bf16 v[32:47], v[112:115], v[128:131], v[32:47]
	ds_read_b64_tr_b16 v[128:129], v187 offset:0x3600
	ds_read_b64_tr_b16 v[130:131], v187 offset:0x3e00
	s_waitcnt lgkmcnt(0)
	v_mfma_f32_32x32x16_bf16 v[16:31], v[100:103], v[116:119], v[16:31]
	v_max_f32_e32 v100, v81, v81
	v_max_f32_e32 v101, v80, v80
	v_max_f32_e32 v100, v101, v100
	v_max3_f32 v100, v100, v82, v83
	v_max3_f32 v100, v100, v84, v85
	v_max3_f32 v100, v100, v86, v87
	v_max3_f32 v100, v100, v88, v89
	v_max3_f32 v100, v100, v90, v91
	v_max3_f32 v100, v100, v92, v93
	v_mfma_f32_32x32x16_bf16 v[16:31], v[104:107], v[120:123], v[16:31]
	v_max3_f32 v100, v100, v94, v95
	v_max3_f32 v100, v100, v64, v65
	v_max3_f32 v100, v100, v66, v67
	v_max3_f32 v100, v100, v68, v69
	v_max3_f32 v100, v100, v70, v71
	v_max3_f32 v100, v100, v72, v73
	v_max3_f32 v100, v100, v74, v75
	v_max3_f32 v100, v100, v76, v77
	v_mfma_f32_32x32x16_bf16 v[16:31], v[108:111], v[124:127], v[16:31]
	v_max3_f32 v100, v100, v78, v79
	v_mov_b32_e32 v101, v100
	s_nop 1
	v_permlane32_swap_b32_e32 v100, v101
	v_max_f32_e32 v101, v101, v101
	v_max_f32_e32 v100, v100, v100
	v_max_f32_e32 v100, v100, v101
	v_sub_f32_e32 v101, v100, v150
	v_cmp_ge_f32_e32 vcc, s87, v101
	v_max_f32_e32 v101, v150, v150
	v_max_f32_e32 v101, v101, v100
	v_mfma_f32_32x32x16_bf16 v[16:31], v[112:115], v[128:131], v[16:31]
	v_sub_f32_e32 v100, v150, v101
	v_mul_f32_e32 v100, 0x3e0293ee, v100
	v_exp_f32_e32 v100, v100
	s_cmp_eq_u64 vcc, exec
	s_cselect_b64 s[42:43], -1, 0
	v_cndmask_b32_e64 v100, v100, 1.0, s[42:43]
	v_cmp_gt_f32_e32 vcc, 1.0, v100
	s_waitcnt vmcnt(0)
	s_barrier
	s_cbranch_vccz .LBB0_470
	s_and_saveexec_b64 s[6:7], s[40:41]
	ds_write_b32 v184, v100 offset:128
	s_or_b64 exec, exec, s[6:7]
	s_waitcnt lgkmcnt(0)
	v_add_u32_e32 v114, v183, v96
	ds_read_b128 v[102:105], v114 offset:224
	ds_read_b128 v[106:109], v114 offset:192
	ds_read_b128 v[110:113], v114 offset:160
	ds_read_b128 v[114:117], v114 offset:128
	s_waitcnt lgkmcnt(3)
	v_pk_mul_f32 v[12:13], v[12:13], v[102:103]
	s_waitcnt lgkmcnt(2)
	v_pk_mul_f32 v[8:9], v[8:9], v[106:107]
	s_waitcnt lgkmcnt(1)
	v_pk_mul_f32 v[4:5], v[4:5], v[110:111]
	v_pk_mul_f32 v[14:15], v[14:15], v[104:105]
	v_pk_mul_f32 v[10:11], v[10:11], v[108:109]
	v_pk_mul_f32 v[6:7], v[6:7], v[112:113]
	s_waitcnt lgkmcnt(0)
	v_pk_mul_f32 v[2:3], v[2:3], v[116:117]
	v_pk_mul_f32 v[0:1], v[0:1], v[114:115]
	v_pk_mul_f32 v[60:61], v[60:61], v[102:103]
	v_pk_mul_f32 v[56:57], v[56:57], v[106:107]
	v_pk_mul_f32 v[52:53], v[52:53], v[110:111]
	v_pk_mul_f32 v[62:63], v[62:63], v[104:105]
	v_pk_mul_f32 v[58:59], v[58:59], v[108:109]
	v_pk_mul_f32 v[54:55], v[54:55], v[112:113]
	v_pk_mul_f32 v[50:51], v[50:51], v[116:117]
	v_pk_mul_f32 v[48:49], v[48:49], v[114:115]
	v_pk_mul_f32 v[44:45], v[44:45], v[102:103]
	v_pk_mul_f32 v[40:41], v[40:41], v[106:107]
	v_pk_mul_f32 v[36:37], v[36:37], v[110:111]
	v_pk_mul_f32 v[46:47], v[46:47], v[104:105]
	v_pk_mul_f32 v[42:43], v[42:43], v[108:109]
	v_pk_mul_f32 v[38:39], v[38:39], v[112:113]
	v_pk_mul_f32 v[34:35], v[34:35], v[116:117]
	v_pk_mul_f32 v[32:33], v[32:33], v[114:115]
	v_pk_mul_f32 v[28:29], v[28:29], v[102:103]
	v_pk_mul_f32 v[24:25], v[24:25], v[106:107]
	v_pk_mul_f32 v[20:21], v[20:21], v[110:111]
	v_pk_mul_f32 v[30:31], v[30:31], v[104:105]
	v_pk_mul_f32 v[26:27], v[26:27], v[108:109]
	v_pk_mul_f32 v[22:23], v[22:23], v[112:113]
	v_pk_mul_f32 v[18:19], v[18:19], v[116:117]
	v_pk_mul_f32 v[16:17], v[16:17], v[114:115]
